# v56 + 100 six-instruction f32->bf16 RNE packs (bfe/add3/lshr/and_or) replaced by v_cvt_pk_bf16_f32 (GEMM epilogues, LN1/LN2, vt)
# baseline (speedup 1.0000x reference)
; #define LAS __attribute__((address_space(3)))
; __device__ __forceinline__ unsigned pk2(float lo, float hi) { return (unsigned)f2bf(lo) | ((unsigned)f2bf(hi) << 16); }
; __device__ __forceinline__ void tr_finish(const TrItem& t, const float (&v)[32], LAS float* scr, int lane) {
;     const int nblk = t.N / 32, kb = t.item / nblk, nb = t.item % nblk, k0 = 64 * kb, n0 = 32 * nb;
; #pragma unroll
;     for (int i = 0; i < 32; ++i) scr[(2 * i + (lane >> 5)) * 33 + (lane & 31)] = v[i];
;     asm volatile("s_waitcnt lgkmcnt(0)" ::: "memory");
;     const int c = lane & 7;
; #pragma unroll
;     for (int j = 0; j < 4; ++j) { const int n = (lane >> 3) + 8 * j; const LAS float* s = scr + (8 * c) * 33 + n;
;         u32x4 o; o.x = pk2(s[0 * 33], s[1 * 33]); o.y = pk2(s[2 * 33], s[3 * 33]); o.z = pk2(s[4 * 33], s[5 * 33]); o.w = pk2(s[6 * 33], s[7 * 33]);
;         const int ng = n0 + n; const int row = t.mode == 0 ? ng : (8 * (ng >> 2) + (ng & 3) + (t.mode == 2 ? 4 : 0));
;         *(u32x4*)(t.WT + (size_t)row * t.K + k0 + 8 * c) = o; }
.LBB0_245:
	s_or_b64 exec, exec, s[22:23]
	v_cvt_f32_i32_sdwa v40, sext(v116) dst_sel:DWORD dst_unused:UNUSED_PAD src0_sel:WORD_0
	v_cvt_f32_i32_sdwa v117, sext(v115) dst_sel:DWORD dst_unused:UNUSED_PAD src0_sel:WORD_0
	s_waitcnt vmcnt(0)
	ds_write2_b32 v82, v2, v3 offset1:66
	v_xor_b32_sdwa v41, sext(v115), sext(v116) dst_sel:DWORD dst_unused:UNUSED_PAD src0_sel:WORD_0 src1_sel:WORD_0
	v_rcp_iflag_f32_e32 v2, v40
	ds_write2_b32 v82, v4, v5 offset0:132 offset1:198
	v_ashrrev_i32_e32 v3, 30, v41
	v_or_b32_e32 v3, 1, v3
	v_mul_f32_e32 v2, v117, v2
	v_trunc_f32_e32 v2, v2
	v_cvt_i32_f32_e32 v4, v2
	v_fma_f32 v2, -v2, v40, v117
	v_cmp_ge_f32_e64 vcc, |v2|, |v40|
	v_add_u32_e32 v42, s81, v42
	s_nop 0
	v_cndmask_b32_e32 v2, 0, v3, vcc
	v_add_u32_e32 v2, v4, v2
	v_mov_b32_e32 v3, 6
	v_lshlrev_b32_sdwa v40, v3, sext(v2) dst_sel:DWORD dst_unused:UNUSED_PAD src0_sel:DWORD src1_sel:WORD_0
	v_add_u32_e32 v3, 0x400, v82
	ds_write2_b32 v3, v6, v7 offset0:8 offset1:74
	ds_write2_b32 v3, v8, v9 offset0:140 offset1:206
	v_add_u32_e32 v3, 0x800, v82
	ds_write2_b32 v3, v10, v11 offset0:16 offset1:82
	ds_write2_b32 v3, v12, v13 offset0:148 offset1:214
	v_add_u32_e32 v3, 0xc00, v82
	ds_write2_b32 v3, v14, v15 offset0:24 offset1:90
	ds_write2_b32 v3, v16, v17 offset0:156 offset1:222
	v_add_u32_e32 v3, 0x1000, v82
	ds_write2_b32 v3, v18, v19 offset0:32 offset1:98
	ds_write2_b32 v3, v20, v21 offset0:164 offset1:230
	v_add_u32_e32 v3, 0x1400, v82
	ds_write2_b32 v3, v22, v23 offset0:40 offset1:106
	ds_write2_b32 v3, v24, v25 offset0:172 offset1:238
	v_add_u32_e32 v3, 0x1800, v82
	ds_write2_b32 v3, v26, v27 offset0:48 offset1:114
	ds_write2_b32 v3, v28, v29 offset0:180 offset1:246
	v_add_u32_e32 v3, 0x1c00, v82
	ds_write2_b32 v3, v30, v31 offset0:56 offset1:122
	ds_write2_b32 v3, v32, v33 offset0:188 offset1:254
	s_waitcnt lgkmcnt(0)
	ds_read2_b32 v[6:7], v78 offset1:8
	ds_read2_b32 v[8:9], v78 offset0:33 offset1:41
	v_mul_lo_u16_e32 v2, v2, v116
	ds_read2_b32 v[10:11], v78 offset0:66 offset1:74
	v_sub_u16_e32 v2, v115, v2
	ds_read2_b32 v[12:13], v78 offset0:99 offset1:107
	v_lshlrev_b32_sdwa v26, v252, sext(v2) dst_sel:DWORD dst_unused:UNUSED_PAD src0_sel:DWORD src1_sel:WORD_0
	s_waitcnt lgkmcnt(0)
	ds_read2_b32 v[14:15], v78 offset0:132 offset1:140
	ds_read2_b32 v[16:17], v78 offset0:165 offset1:173
	v_cvt_pk_bf16_f32 v2, v6, v8
	ds_read2_b32 v[18:19], v78 offset0:198 offset1:206
	ds_read2_b32 v[20:21], v78 offset0:231 offset1:239
	v_cvt_pk_bf16_f32 v3, v10, v12
	s_waitcnt lgkmcnt(3)
	s_waitcnt lgkmcnt(2)
	v_cvt_pk_bf16_f32 v4, v14, v16
	s_waitcnt lgkmcnt(1)
	s_waitcnt lgkmcnt(0)
	v_cvt_pk_bf16_f32 v5, v18, v20
	v_or_b32_e32 v6, v26, v76
	v_lshlrev_b32_e32 v8, 1, v6
	v_and_b32_e32 v8, 0xffffffc8, v8
	v_or3_b32 v8, v77, v8, v114
	v_cndmask_b32_e64 v6, v8, v6, s[20:21]
	v_ashrrev_i32_e32 v8, 31, v6
	v_mul_lo_u32 v8, v38, v8
	v_mul_lo_u32 v10, v39, v6
	v_mad_u64_u32 v[22:23], s[22:23], v38, v6, 0
	v_ashrrev_i32_e32 v41, 31, v40
	v_add3_u32 v23, v23, v8, v10
	v_lshl_add_u64 v[22:23], v[22:23], 1, v[36:37]
	v_lshlrev_b64 v[24:25], 1, v[40:41]
	v_lshl_add_u64 v[22:23], v[22:23], 0, v[24:25]
	v_lshl_add_u64 v[22:23], v[22:23], 0, v[0:1]
	global_store_dwordx4 v[22:23], v[2:5], off
	v_bfe_u32 v6, v21, 16, 1
	v_add3_u32 v6, v21, v6, s79
	v_cvt_pk_bf16_f32 v2, v7, v9
	v_cvt_pk_bf16_f32 v3, v11, v13
	v_cvt_pk_bf16_f32 v4, v15, v17
	v_bfe_u32 v5, v19, 16, 1
	v_add3_u32 v5, v19, v5, s79
	v_lshrrev_b32_e32 v5, 16, v5
	v_and_or_b32 v5, v6, s89, v5
	v_or_b32_e32 v6, v26, v79
	v_lshlrev_b32_e32 v7, 1, v6
	v_and_b32_e32 v7, 0xffffffd8, v7
	v_or3_b32 v7, v77, v7, v114
	v_cndmask_b32_e64 v6, v7, v6, s[20:21]
	v_ashrrev_i32_e32 v7, 31, v6
	v_mul_lo_u32 v8, v38, v7
	v_mul_lo_u32 v9, v39, v6
	v_mad_u64_u32 v[6:7], s[22:23], v38, v6, 0
	v_add3_u32 v7, v7, v8, v9
	v_lshl_add_u64 v[6:7], v[6:7], 1, v[36:37]
	v_lshl_add_u64 v[6:7], v[6:7], 0, v[24:25]
	ds_read2_b32 v[8:9], v78 offset0:16 offset1:24
	v_lshl_add_u64 v[6:7], v[6:7], 0, v[0:1]
	global_store_dwordx4 v[6:7], v[2:5], off
	ds_read2_b32 v[6:7], v78 offset0:49 offset1:57
	ds_read2_b32 v[10:11], v78 offset0:82 offset1:90
	ds_read2_b32 v[12:13], v78 offset0:115 offset1:123
	s_waitcnt lgkmcnt(3)
; #define LAS __attribute__((address_space(3)))
; __device__ __forceinline__ unsigned pk2(float lo, float hi) { return (unsigned)f2bf(lo) | ((unsigned)f2bf(hi) << 16); }
; __device__ __forceinline__ void tr_finish(const TrItem& t, const float (&v)[32], LAS float* scr, int lane) {
;     ...
;     for (int j = 0; j < 4; ++j) { const int n = (lane >> 3) + 8 * j; const LAS float* s = scr + (8 * c) * 33 + n;
;         u32x4 o; o.x = pk2(s[0 * 33], s[1 * 33]); o.y = pk2(s[2 * 33], s[3 * 33]); o.z = pk2(s[4 * 33], s[5 * 33]); o.w = pk2(s[6 * 33], s[7 * 33]);
;         const int ng = n0 + n; const int row = t.mode == 0 ? ng : (8 * (ng >> 2) + (ng & 3) + (t.mode == 2 ? 4 : 0));
;         *(u32x4*)(t.WT + (size_t)row * t.K + k0 + 8 * c) = o; }
; template <int GRP> __device__ __forceinline__ void tr_group(const Params& p, unsigned char* ws, LAS float* scr, int lane, int start, int stride) {
;     ...
;     while (g < N) { const int g2 = g + 2 * stride;
;         if (g2 < N) { const TrItem tn = tr_decode(p, ws, tr_index<GRP>(g2)); tr_load(tn, nx2, lane); }
;         const TrItem tc = tr_decode(p, ws, tr_index<GRP>(g)); tr_finish(tc, cur, scr, lane);
; #pragma unroll
;         for (int i = 0; i < 32; ++i) { cur[i] = nx1[i]; nx1[i] = nx2[i]; }
;         g += stride; }
	s_waitcnt lgkmcnt(2)
	ds_read2_b32 v[14:15], v78 offset0:148 offset1:156
	ds_read2_b32 v[16:17], v78 offset0:181 offset1:189
	v_cvt_pk_bf16_f32 v2, v8, v6
	s_waitcnt lgkmcnt(3)
	s_waitcnt lgkmcnt(2)
	ds_read2_b32 v[18:19], v78 offset0:214 offset1:222
	ds_read2_b32 v[20:21], v78 offset0:247 offset1:255
	v_cvt_pk_bf16_f32 v3, v10, v12
	s_waitcnt lgkmcnt(3)
	s_waitcnt lgkmcnt(2)
	v_cvt_pk_bf16_f32 v4, v14, v16
	s_waitcnt lgkmcnt(1)
	s_waitcnt lgkmcnt(0)
	v_cvt_pk_bf16_f32 v5, v18, v20
	v_or_b32_e32 v6, v26, v80
	v_lshlrev_b32_e32 v8, 1, v6
	v_and_b32_e32 v8, 0xffffffe8, v8
	v_or3_b32 v8, v77, v8, v114
	v_cndmask_b32_e64 v6, v8, v6, s[20:21]
	v_ashrrev_i32_e32 v8, 31, v6
	v_mul_lo_u32 v8, v38, v8
	v_mul_lo_u32 v10, v39, v6
	v_mad_u64_u32 v[22:23], s[22:23], v38, v6, 0
	v_add3_u32 v23, v23, v8, v10
	v_lshl_add_u64 v[22:23], v[22:23], 1, v[36:37]
	v_lshl_add_u64 v[22:23], v[22:23], 0, v[24:25]
	v_lshl_add_u64 v[22:23], v[22:23], 0, v[0:1]
	global_store_dwordx4 v[22:23], v[2:5], off
	v_bfe_u32 v6, v21, 16, 1
	v_add3_u32 v6, v21, v6, s79
	v_cvt_pk_bf16_f32 v2, v9, v7
	v_cvt_pk_bf16_f32 v3, v11, v13
	v_cvt_pk_bf16_f32 v4, v15, v17
	v_bfe_u32 v5, v19, 16, 1
	v_add3_u32 v5, v19, v5, s79
	v_lshrrev_b32_e32 v5, 16, v5
	v_and_or_b32 v5, v6, s89, v5
	v_or_b32_e32 v6, v26, v81
	v_lshlrev_b32_e32 v7, 1, v6
	v_and_b32_e32 v7, -8, v7
	v_or3_b32 v7, v77, v7, v114
	v_cndmask_b32_e64 v6, v7, v6, s[20:21]
	v_ashrrev_i32_e32 v7, 31, v6
	v_mul_lo_u32 v8, v38, v7
	v_mul_lo_u32 v9, v39, v6
	v_mad_u64_u32 v[6:7], s[20:21], v38, v6, 0
	v_add3_u32 v7, v7, v8, v9
	v_lshl_add_u64 v[6:7], v[6:7], 1, v[36:37]
	v_lshl_add_u64 v[6:7], v[6:7], 0, v[24:25]
	v_lshl_add_u64 v[6:7], v[6:7], 0, v[0:1]
	global_store_dwordx4 v[6:7], v[2:5], off
	s_waitcnt lgkmcnt(0)
	s_movk_i32 s20, 0xfff
	v_cmp_lt_i32_e32 vcc, s20, v42
	v_mov_b32_e32 v2, v43
	v_mov_b32_e32 v3, v44
	v_mov_b32_e32 v4, v45
	v_mov_b32_e32 v5, v46
	v_mov_b32_e32 v6, v47
	v_mov_b32_e32 v7, v48
	v_mov_b32_e32 v8, v49
	v_mov_b32_e32 v9, v50
	v_mov_b32_e32 v10, v51
	v_mov_b32_e32 v11, v52
	v_mov_b32_e32 v12, v53
	v_mov_b32_e32 v13, v54
	v_mov_b32_e32 v14, v55
	v_mov_b32_e32 v15, v56
	v_mov_b32_e32 v16, v57
	v_mov_b32_e32 v17, v58
	v_mov_b32_e32 v18, v59
	v_mov_b32_e32 v19, v60
	v_mov_b32_e32 v20, v61
	v_mov_b32_e32 v21, v62
	v_mov_b32_e32 v22, v63
	v_mov_b32_e32 v23, v64
	v_mov_b32_e32 v24, v65
	v_mov_b32_e32 v25, v66
	v_mov_b32_e32 v26, v67
	v_mov_b32_e32 v27, v68
	v_mov_b32_e32 v28, v69
	v_mov_b32_e32 v29, v70
	v_mov_b32_e32 v30, v71
	v_mov_b32_e32 v31, v72
	v_mov_b32_e32 v32, v73
	v_mov_b32_e32 v33, v74
	s_or_b64 s[18:19], vcc, s[18:19]
	v_mov_b32_e32 v74, v113
	v_mov_b32_e32 v73, v112
	v_mov_b32_e32 v72, v111
	v_mov_b32_e32 v71, v110
	v_mov_b32_e32 v70, v109
	v_mov_b32_e32 v69, v108
	v_mov_b32_e32 v68, v107
	v_mov_b32_e32 v67, v106
	v_mov_b32_e32 v66, v105
	v_mov_b32_e32 v65, v104
	v_mov_b32_e32 v64, v103
	v_mov_b32_e32 v63, v102
	v_mov_b32_e32 v62, v101
	v_mov_b32_e32 v61, v100
	v_mov_b32_e32 v60, v99
	v_mov_b32_e32 v59, v98
	v_mov_b32_e32 v58, v97
	v_mov_b32_e32 v57, v96
	v_mov_b32_e32 v56, v95
	v_mov_b32_e32 v55, v94
	v_mov_b32_e32 v54, v93
	v_mov_b32_e32 v53, v92
	v_mov_b32_e32 v52, v91
	v_mov_b32_e32 v51, v90
	v_mov_b32_e32 v50, v89
	v_mov_b32_e32 v49, v88
	v_mov_b32_e32 v48, v87
	v_mov_b32_e32 v47, v86
	v_mov_b32_e32 v46, v85
	v_mov_b32_e32 v45, v84
	v_mov_b32_e32 v44, v83
	v_mov_b32_e32 v43, v35
	s_andn2_b64 exec, exec, s[18:19]
	s_cbranch_execz .LBB0_280

; #define LAS __attribute__((address_space(3)))
; __device__ __forceinline__ unsigned pk2(float lo, float hi) { return (unsigned)f2bf(lo) | ((unsigned)f2bf(hi) << 16); }
; __device__ __forceinline__ void tr_finish(const TrItem& t, const float (&v)[32], LAS float* scr, int lane) {
;     const int nblk = t.N / 32, kb = t.item / nblk, nb = t.item % nblk, k0 = 64 * kb, n0 = 32 * nb;
; #pragma unroll
;     for (int i = 0; i < 32; ++i) scr[(2 * i + (lane >> 5)) * 33 + (lane & 31)] = v[i];
;     asm volatile("s_waitcnt lgkmcnt(0)" ::: "memory");
;     const int c = lane & 7;
; #pragma unroll
;     for (int j = 0; j < 4; ++j) { const int n = (lane >> 3) + 8 * j; const LAS float* s = scr + (8 * c) * 33 + n;
;         u32x4 o; o.x = pk2(s[0 * 33], s[1 * 33]); o.y = pk2(s[2 * 33], s[3 * 33]); o.z = pk2(s[4 * 33], s[5 * 33]); o.w = pk2(s[6 * 33], s[7 * 33]);
;         const int ng = n0 + n; const int row = t.mode == 0 ? ng : (8 * (ng >> 2) + (ng & 3) + (t.mode == 2 ? 4 : 0));
;         *(u32x4*)(t.WT + (size_t)row * t.K + k0 + 8 * c) = o; }
.LBB0_330:
	s_or_b64 exec, exec, s[18:19]
	v_cvt_f32_i32_sdwa v40, sext(v117) dst_sel:DWORD dst_unused:UNUSED_PAD src0_sel:WORD_0
	v_cvt_f32_i32_sdwa v118, sext(v116) dst_sel:DWORD dst_unused:UNUSED_PAD src0_sel:WORD_0
	s_waitcnt vmcnt(0)
	ds_write2_b32 v83, v2, v3 offset1:66
	v_xor_b32_sdwa v41, sext(v116), sext(v117) dst_sel:DWORD dst_unused:UNUSED_PAD src0_sel:WORD_0 src1_sel:WORD_0
	v_rcp_iflag_f32_e32 v2, v40
	ds_write2_b32 v83, v4, v5 offset0:132 offset1:198
	v_ashrrev_i32_e32 v3, 30, v41
	v_or_b32_e32 v3, 1, v3
	v_mul_f32_e32 v2, v118, v2
	v_trunc_f32_e32 v2, v2
	v_cvt_i32_f32_e32 v4, v2
	v_fma_f32 v2, -v2, v40, v118
	v_cmp_ge_f32_e64 vcc, |v2|, |v40|
	v_add_u32_e32 v81, s81, v81
	v_add_u32_e32 v82, s81, v82
	v_cndmask_b32_e32 v2, 0, v3, vcc
	v_add_u32_e32 v2, v4, v2
	v_mov_b32_e32 v3, 6
	v_lshlrev_b32_sdwa v40, v3, sext(v2) dst_sel:DWORD dst_unused:UNUSED_PAD src0_sel:DWORD src1_sel:WORD_0
	v_add_u32_e32 v3, 0x400, v83
	ds_write2_b32 v3, v6, v7 offset0:8 offset1:74
	ds_write2_b32 v3, v8, v9 offset0:140 offset1:206
	v_add_u32_e32 v3, 0x800, v83
	ds_write2_b32 v3, v10, v11 offset0:16 offset1:82
	ds_write2_b32 v3, v12, v13 offset0:148 offset1:214
	v_add_u32_e32 v3, 0xc00, v83
	ds_write2_b32 v3, v14, v15 offset0:24 offset1:90
	ds_write2_b32 v3, v16, v17 offset0:156 offset1:222
	v_add_u32_e32 v3, 0x1000, v83
	ds_write2_b32 v3, v18, v19 offset0:32 offset1:98
	ds_write2_b32 v3, v20, v21 offset0:164 offset1:230
	v_add_u32_e32 v3, 0x1400, v83
	ds_write2_b32 v3, v22, v23 offset0:40 offset1:106
	ds_write2_b32 v3, v24, v25 offset0:172 offset1:238
	v_add_u32_e32 v3, 0x1800, v83
	ds_write2_b32 v3, v26, v27 offset0:48 offset1:114
	ds_write2_b32 v3, v28, v29 offset0:180 offset1:246
	v_add_u32_e32 v3, 0x1c00, v83
	ds_write2_b32 v3, v30, v31 offset0:56 offset1:122
	ds_write2_b32 v3, v32, v33 offset0:188 offset1:254
	s_waitcnt lgkmcnt(0)
	ds_read2_b32 v[6:7], v77 offset1:8
	ds_read2_b32 v[8:9], v77 offset0:33 offset1:41
	v_mul_lo_u16_e32 v2, v2, v117
	ds_read2_b32 v[10:11], v77 offset0:66 offset1:74
	v_sub_u16_e32 v2, v116, v2
	ds_read2_b32 v[12:13], v77 offset0:99 offset1:107
	v_lshlrev_b32_sdwa v26, v252, sext(v2) dst_sel:DWORD dst_unused:UNUSED_PAD src0_sel:DWORD src1_sel:WORD_0
	s_waitcnt lgkmcnt(0)
	ds_read2_b32 v[14:15], v77 offset0:132 offset1:140
	ds_read2_b32 v[16:17], v77 offset0:165 offset1:173
	v_cvt_pk_bf16_f32 v2, v6, v8
	ds_read2_b32 v[18:19], v77 offset0:198 offset1:206
	ds_read2_b32 v[20:21], v77 offset0:231 offset1:239
	v_cvt_pk_bf16_f32 v3, v10, v12
	s_waitcnt lgkmcnt(3)
	s_waitcnt lgkmcnt(2)
	v_cvt_pk_bf16_f32 v4, v14, v16
	s_waitcnt lgkmcnt(1)
	s_waitcnt lgkmcnt(0)
	v_cvt_pk_bf16_f32 v5, v18, v20
	v_or_b32_e32 v6, v26, v75
	v_lshlrev_b32_e32 v8, 1, v6
	v_and_b32_e32 v8, 0xffffffc8, v8
	v_or3_b32 v8, v76, v8, v115
	v_cndmask_b32_e64 v6, v8, v6, s[16:17]
	v_ashrrev_i32_e32 v8, 31, v6
	v_mul_lo_u32 v8, v38, v8
	v_mul_lo_u32 v10, v39, v6
	v_mad_u64_u32 v[22:23], s[18:19], v38, v6, 0
	v_ashrrev_i32_e32 v41, 31, v40
	v_add3_u32 v23, v23, v8, v10
	v_lshl_add_u64 v[22:23], v[22:23], 1, v[36:37]
	v_lshlrev_b64 v[24:25], 1, v[40:41]
	v_lshl_add_u64 v[22:23], v[22:23], 0, v[24:25]
	v_lshl_add_u64 v[22:23], v[22:23], 0, v[0:1]
	global_store_dwordx4 v[22:23], v[2:5], off
	v_bfe_u32 v6, v21, 16, 1
	v_add3_u32 v6, v21, v6, s79
	v_cvt_pk_bf16_f32 v2, v7, v9
	v_cvt_pk_bf16_f32 v3, v11, v13
	v_cvt_pk_bf16_f32 v4, v15, v17
	v_bfe_u32 v5, v19, 16, 1
	v_add3_u32 v5, v19, v5, s79
	v_lshrrev_b32_e32 v5, 16, v5
	v_and_or_b32 v5, v6, s89, v5
	v_or_b32_e32 v6, v26, v78
	v_lshlrev_b32_e32 v7, 1, v6
	v_and_b32_e32 v7, 0xffffffd8, v7
	v_or3_b32 v7, v76, v7, v115
	v_cndmask_b32_e64 v6, v7, v6, s[16:17]
	v_ashrrev_i32_e32 v7, 31, v6
	v_mul_lo_u32 v8, v38, v7
	v_mul_lo_u32 v9, v39, v6
	v_mad_u64_u32 v[6:7], s[18:19], v38, v6, 0
	v_add3_u32 v7, v7, v8, v9
	v_lshl_add_u64 v[6:7], v[6:7], 1, v[36:37]
	v_lshl_add_u64 v[6:7], v[6:7], 0, v[24:25]
	ds_read2_b32 v[8:9], v77 offset0:16 offset1:24
	v_lshl_add_u64 v[6:7], v[6:7], 0, v[0:1]
	global_store_dwordx4 v[6:7], v[2:5], off
	ds_read2_b32 v[6:7], v77 offset0:49 offset1:57
	ds_read2_b32 v[10:11], v77 offset0:82 offset1:90
	ds_read2_b32 v[12:13], v77 offset0:115 offset1:123
	s_waitcnt lgkmcnt(3)
; #define LAS __attribute__((address_space(3)))
; __device__ __forceinline__ unsigned pk2(float lo, float hi) { return (unsigned)f2bf(lo) | ((unsigned)f2bf(hi) << 16); }
; __device__ __forceinline__ void tr_finish(const TrItem& t, const float (&v)[32], LAS float* scr, int lane) {
;     ...
;     for (int j = 0; j < 4; ++j) { const int n = (lane >> 3) + 8 * j; const LAS float* s = scr + (8 * c) * 33 + n;
;         u32x4 o; o.x = pk2(s[0 * 33], s[1 * 33]); o.y = pk2(s[2 * 33], s[3 * 33]); o.z = pk2(s[4 * 33], s[5 * 33]); o.w = pk2(s[6 * 33], s[7 * 33]);
;         const int ng = n0 + n; const int row = t.mode == 0 ? ng : (8 * (ng >> 2) + (ng & 3) + (t.mode == 2 ? 4 : 0));
;         *(u32x4*)(t.WT + (size_t)row * t.K + k0 + 8 * c) = o; }
; template <int GRP> __device__ __forceinline__ void tr_group(const Params& p, unsigned char* ws, LAS float* scr, int lane, int start, int stride) {
;     ...
;     while (g < N) { const int g2 = g + 2 * stride;
;         if (g2 < N) { const TrItem tn = tr_decode(p, ws, tr_index<GRP>(g2)); tr_load(tn, nx2, lane); }
;         const TrItem tc = tr_decode(p, ws, tr_index<GRP>(g)); tr_finish(tc, cur, scr, lane);
; #pragma unroll
;         for (int i = 0; i < 32; ++i) { cur[i] = nx1[i]; nx1[i] = nx2[i]; }
;         g += stride; }
	s_waitcnt lgkmcnt(2)
	ds_read2_b32 v[14:15], v77 offset0:148 offset1:156
	ds_read2_b32 v[16:17], v77 offset0:181 offset1:189
	v_cvt_pk_bf16_f32 v2, v8, v6
	s_waitcnt lgkmcnt(3)
	s_waitcnt lgkmcnt(2)
	ds_read2_b32 v[18:19], v77 offset0:214 offset1:222
	ds_read2_b32 v[20:21], v77 offset0:247 offset1:255
	v_cvt_pk_bf16_f32 v3, v10, v12
	s_waitcnt lgkmcnt(3)
	s_waitcnt lgkmcnt(2)
	v_cvt_pk_bf16_f32 v4, v14, v16
	s_waitcnt lgkmcnt(1)
	s_waitcnt lgkmcnt(0)
	v_cvt_pk_bf16_f32 v5, v18, v20
	v_or_b32_e32 v6, v26, v79
	v_lshlrev_b32_e32 v8, 1, v6
	v_and_b32_e32 v8, 0xffffffe8, v8
	v_or3_b32 v8, v76, v8, v115
	v_cndmask_b32_e64 v6, v8, v6, s[16:17]
	v_ashrrev_i32_e32 v8, 31, v6
	v_mul_lo_u32 v8, v38, v8
	v_mul_lo_u32 v10, v39, v6
	v_mad_u64_u32 v[22:23], s[18:19], v38, v6, 0
	v_add3_u32 v23, v23, v8, v10
	v_lshl_add_u64 v[22:23], v[22:23], 1, v[36:37]
	v_lshl_add_u64 v[22:23], v[22:23], 0, v[24:25]
	v_lshl_add_u64 v[22:23], v[22:23], 0, v[0:1]
	global_store_dwordx4 v[22:23], v[2:5], off
	v_bfe_u32 v6, v21, 16, 1
	v_add3_u32 v6, v21, v6, s79
	v_cvt_pk_bf16_f32 v2, v9, v7
	v_cvt_pk_bf16_f32 v3, v11, v13
	v_cvt_pk_bf16_f32 v4, v15, v17
	v_bfe_u32 v5, v19, 16, 1
	v_add3_u32 v5, v19, v5, s79
	v_lshrrev_b32_e32 v5, 16, v5
	v_and_or_b32 v5, v6, s89, v5
	v_or_b32_e32 v6, v26, v80
	v_lshlrev_b32_e32 v7, 1, v6
	v_and_b32_e32 v7, -8, v7
	v_or3_b32 v7, v76, v7, v115
	v_cndmask_b32_e64 v6, v7, v6, s[16:17]
	v_ashrrev_i32_e32 v7, 31, v6
	v_mul_lo_u32 v8, v38, v7
	v_mul_lo_u32 v9, v39, v6
	v_mad_u64_u32 v[6:7], s[16:17], v38, v6, 0
	v_add3_u32 v7, v7, v8, v9
	v_lshl_add_u64 v[6:7], v[6:7], 1, v[36:37]
	v_lshl_add_u64 v[6:7], v[6:7], 0, v[24:25]
	v_lshl_add_u64 v[6:7], v[6:7], 0, v[0:1]
	global_store_dwordx4 v[6:7], v[2:5], off
	s_waitcnt lgkmcnt(0)
	v_add_u32_e32 v36, s26, v81
	s_movk_i32 s16, 0x9ff
	v_cmp_lt_i32_e32 vcc, s16, v36
	v_mov_b32_e32 v2, v42
	v_mov_b32_e32 v3, v43
	v_mov_b32_e32 v4, v44
	v_mov_b32_e32 v5, v45
	v_mov_b32_e32 v6, v46
	v_mov_b32_e32 v7, v47
	v_mov_b32_e32 v8, v48
	v_mov_b32_e32 v9, v49
	v_mov_b32_e32 v10, v50
	v_mov_b32_e32 v11, v51
	v_mov_b32_e32 v12, v52
	v_mov_b32_e32 v13, v53
	v_mov_b32_e32 v14, v54
	v_mov_b32_e32 v15, v55
	v_mov_b32_e32 v16, v56
	v_mov_b32_e32 v17, v57
	v_mov_b32_e32 v18, v58
	v_mov_b32_e32 v19, v59
	v_mov_b32_e32 v20, v60
	v_mov_b32_e32 v21, v61
	v_mov_b32_e32 v22, v62
	v_mov_b32_e32 v23, v63
	v_mov_b32_e32 v24, v64
	v_mov_b32_e32 v25, v65
	v_mov_b32_e32 v26, v66
	v_mov_b32_e32 v27, v67
	v_mov_b32_e32 v28, v68
	v_mov_b32_e32 v29, v69
	v_mov_b32_e32 v30, v70
	v_mov_b32_e32 v31, v71
	v_mov_b32_e32 v32, v72
	v_mov_b32_e32 v33, v73
	s_or_b64 s[10:11], vcc, s[10:11]
	v_mov_b32_e32 v73, v114
	v_mov_b32_e32 v72, v113
	v_mov_b32_e32 v71, v112
	v_mov_b32_e32 v70, v111
	v_mov_b32_e32 v69, v110
	v_mov_b32_e32 v68, v109
	v_mov_b32_e32 v67, v108
	v_mov_b32_e32 v66, v107
	v_mov_b32_e32 v65, v106
	v_mov_b32_e32 v64, v105
	v_mov_b32_e32 v63, v104
	v_mov_b32_e32 v62, v103
	v_mov_b32_e32 v61, v102
	v_mov_b32_e32 v60, v101
	v_mov_b32_e32 v59, v100
	v_mov_b32_e32 v58, v99
	v_mov_b32_e32 v57, v98
	v_mov_b32_e32 v56, v97
	v_mov_b32_e32 v55, v96
	v_mov_b32_e32 v54, v95
	v_mov_b32_e32 v53, v94
	v_mov_b32_e32 v52, v93
	v_mov_b32_e32 v51, v92
	v_mov_b32_e32 v50, v91
	v_mov_b32_e32 v49, v90
	v_mov_b32_e32 v48, v89
	v_mov_b32_e32 v47, v88
	v_mov_b32_e32 v46, v87
	v_mov_b32_e32 v45, v86
	v_mov_b32_e32 v44, v85
	v_mov_b32_e32 v43, v84
	v_mov_b32_e32 v42, v35
	s_andn2_b64 exec, exec, s[10:11]
	s_cbranch_execz .LBB0_373

; #define LAS __attribute__((address_space(3)))
; __device__ __forceinline__ unsigned pk2(float lo, float hi) { return (unsigned)f2bf(lo) | ((unsigned)f2bf(hi) << 16); }
; __device__ __forceinline__ void tr_finish(const TrItem& t, const float (&v)[32], LAS float* scr, int lane) {
;     const int nblk = t.N / 32, kb = t.item / nblk, nb = t.item % nblk, k0 = 64 * kb, n0 = 32 * nb;
; #pragma unroll
;     for (int i = 0; i < 32; ++i) scr[(2 * i + (lane >> 5)) * 33 + (lane & 31)] = v[i];
;     asm volatile("s_waitcnt lgkmcnt(0)" ::: "memory");
;     const int c = lane & 7;
; #pragma unroll
;     for (int j = 0; j < 4; ++j) { const int n = (lane >> 3) + 8 * j; const LAS float* s = scr + (8 * c) * 33 + n;
;         u32x4 o; o.x = pk2(s[0 * 33], s[1 * 33]); o.y = pk2(s[2 * 33], s[3 * 33]); o.z = pk2(s[4 * 33], s[5 * 33]); o.w = pk2(s[6 * 33], s[7 * 33]);
;         const int ng = n0 + n; const int row = t.mode == 0 ? ng : (8 * (ng >> 2) + (ng & 3) + (t.mode == 2 ? 4 : 0));
;         *(u32x4*)(t.WT + (size_t)row * t.K + k0 + 8 * c) = o; }
.LBB0_692:
	s_or_b64 exec, exec, s[18:19]
	v_cvt_f32_i32_sdwa v40, sext(v116) dst_sel:DWORD dst_unused:UNUSED_PAD src0_sel:WORD_0
	v_cvt_f32_i32_sdwa v117, sext(v115) dst_sel:DWORD dst_unused:UNUSED_PAD src0_sel:WORD_0
	ds_write2_b32 v82, v2, v3 offset1:66
	v_xor_b32_sdwa v41, sext(v115), sext(v116) dst_sel:DWORD dst_unused:UNUSED_PAD src0_sel:WORD_0 src1_sel:WORD_0
	v_rcp_iflag_f32_e32 v2, v40
	ds_write2_b32 v82, v4, v5 offset0:132 offset1:198
	v_ashrrev_i32_e32 v3, 30, v41
	v_or_b32_e32 v3, 1, v3
	v_mul_f32_e32 v2, v117, v2
	v_trunc_f32_e32 v2, v2
	v_cvt_i32_f32_e32 v4, v2
	v_fma_f32 v2, -v2, v40, v117
	v_cmp_ge_f32_e64 vcc, |v2|, |v40|
	v_add_u32_e32 v42, s26, v42
	s_nop 0
	v_cndmask_b32_e32 v2, 0, v3, vcc
	v_add_u32_e32 v2, v4, v2
	v_mov_b32_e32 v3, 6
	v_lshlrev_b32_sdwa v40, v3, sext(v2) dst_sel:DWORD dst_unused:UNUSED_PAD src0_sel:DWORD src1_sel:WORD_0
	v_add_u32_e32 v3, 0x400, v82
	ds_write2_b32 v3, v6, v7 offset0:8 offset1:74
	ds_write2_b32 v3, v8, v9 offset0:140 offset1:206
	v_add_u32_e32 v3, 0x800, v82
	ds_write2_b32 v3, v10, v11 offset0:16 offset1:82
	ds_write2_b32 v3, v12, v13 offset0:148 offset1:214
	v_add_u32_e32 v3, 0xc00, v82
	ds_write2_b32 v3, v14, v15 offset0:24 offset1:90
	ds_write2_b32 v3, v16, v17 offset0:156 offset1:222
	v_add_u32_e32 v3, 0x1000, v82
	ds_write2_b32 v3, v18, v19 offset0:32 offset1:98
	ds_write2_b32 v3, v20, v21 offset0:164 offset1:230
	v_add_u32_e32 v3, 0x1400, v82
	ds_write2_b32 v3, v22, v23 offset0:40 offset1:106
	ds_write2_b32 v3, v24, v25 offset0:172 offset1:238
	v_add_u32_e32 v3, 0x1800, v82
	s_waitcnt vmcnt(6)
	ds_write2_b32 v3, v26, v27 offset0:48 offset1:114
	s_waitcnt vmcnt(4)
	ds_write2_b32 v3, v28, v29 offset0:180 offset1:246
	v_add_u32_e32 v3, 0x1c00, v82
	s_waitcnt vmcnt(2)
	ds_write2_b32 v3, v30, v31 offset0:56 offset1:122
	s_waitcnt vmcnt(0)
	ds_write2_b32 v3, v32, v33 offset0:188 offset1:254
	s_waitcnt lgkmcnt(0)
	ds_read2_b32 v[6:7], v78 offset1:8
	ds_read2_b32 v[8:9], v78 offset0:33 offset1:41
	v_mul_lo_u16_e32 v2, v2, v116
	ds_read2_b32 v[10:11], v78 offset0:66 offset1:74
	v_sub_u16_e32 v2, v115, v2
	ds_read2_b32 v[12:13], v78 offset0:99 offset1:107
	v_lshlrev_b32_sdwa v26, v252, sext(v2) dst_sel:DWORD dst_unused:UNUSED_PAD src0_sel:DWORD src1_sel:WORD_0
	s_waitcnt lgkmcnt(3)
	s_waitcnt lgkmcnt(2)
	ds_read2_b32 v[14:15], v78 offset0:132 offset1:140
	ds_read2_b32 v[16:17], v78 offset0:165 offset1:173
	v_cvt_pk_bf16_f32 v2, v6, v8
	s_waitcnt lgkmcnt(3)
	s_waitcnt lgkmcnt(2)
	ds_read2_b32 v[18:19], v78 offset0:198 offset1:206
	ds_read2_b32 v[20:21], v78 offset0:231 offset1:239
	v_cvt_pk_bf16_f32 v3, v10, v12
	s_waitcnt lgkmcnt(3)
	s_waitcnt lgkmcnt(2)
	v_cvt_pk_bf16_f32 v4, v14, v16
	s_waitcnt lgkmcnt(1)
	s_waitcnt lgkmcnt(0)
	v_cvt_pk_bf16_f32 v5, v18, v20
	v_or_b32_e32 v6, v26, v76
	v_lshlrev_b32_e32 v8, 1, v6
	v_and_b32_e32 v8, 0xffffffc8, v8
	v_or3_b32 v8, v77, v8, v114
	v_cndmask_b32_e64 v6, v8, v6, s[16:17]
	v_ashrrev_i32_e32 v8, 31, v6
	v_mul_lo_u32 v8, v38, v8
	v_mul_lo_u32 v10, v39, v6
	v_mad_u64_u32 v[22:23], s[18:19], v38, v6, 0
	v_ashrrev_i32_e32 v41, 31, v40
	v_add3_u32 v23, v23, v8, v10
	v_lshl_add_u64 v[22:23], v[22:23], 1, v[36:37]
	v_lshlrev_b64 v[24:25], 1, v[40:41]
	v_lshl_add_u64 v[22:23], v[22:23], 0, v[24:25]
	v_lshl_add_u64 v[22:23], v[22:23], 0, v[0:1]
	global_store_dwordx4 v[22:23], v[2:5], off
	v_bfe_u32 v6, v21, 16, 1
	v_add3_u32 v6, v21, v6, s79
	v_cvt_pk_bf16_f32 v2, v7, v9
	v_cvt_pk_bf16_f32 v3, v11, v13
	v_cvt_pk_bf16_f32 v4, v15, v17
	v_bfe_u32 v5, v19, 16, 1
	v_add3_u32 v5, v19, v5, s79
	v_lshrrev_b32_e32 v5, 16, v5
	v_and_or_b32 v5, v6, s89, v5
	v_or_b32_e32 v6, v26, v79
	v_lshlrev_b32_e32 v7, 1, v6
	v_and_b32_e32 v7, 0xffffffd8, v7
	v_or3_b32 v7, v77, v7, v114
	v_cndmask_b32_e64 v6, v7, v6, s[16:17]
	v_ashrrev_i32_e32 v7, 31, v6
	v_mul_lo_u32 v8, v38, v7
	v_mul_lo_u32 v9, v39, v6
	v_mad_u64_u32 v[6:7], s[18:19], v38, v6, 0
	v_add3_u32 v7, v7, v8, v9
	v_lshl_add_u64 v[6:7], v[6:7], 1, v[36:37]
	v_lshl_add_u64 v[6:7], v[6:7], 0, v[24:25]
	ds_read2_b32 v[8:9], v78 offset0:16 offset1:24
	v_lshl_add_u64 v[6:7], v[6:7], 0, v[0:1]
	global_store_dwordx4 v[6:7], v[2:5], off
	ds_read2_b32 v[6:7], v78 offset0:49 offset1:57
	ds_read2_b32 v[10:11], v78 offset0:82 offset1:90
	ds_read2_b32 v[12:13], v78 offset0:115 offset1:123
	s_waitcnt lgkmcnt(3)
; #define LAS __attribute__((address_space(3)))
; __device__ __forceinline__ unsigned pk2(float lo, float hi) { return (unsigned)f2bf(lo) | ((unsigned)f2bf(hi) << 16); }
; __device__ __forceinline__ void tr_finish(const TrItem& t, const float (&v)[32], LAS float* scr, int lane) {
;     ...
;     for (int j = 0; j < 4; ++j) { const int n = (lane >> 3) + 8 * j; const LAS float* s = scr + (8 * c) * 33 + n;
;         u32x4 o; o.x = pk2(s[0 * 33], s[1 * 33]); o.y = pk2(s[2 * 33], s[3 * 33]); o.z = pk2(s[4 * 33], s[5 * 33]); o.w = pk2(s[6 * 33], s[7 * 33]);
;         const int ng = n0 + n; const int row = t.mode == 0 ? ng : (8 * (ng >> 2) + (ng & 3) + (t.mode == 2 ? 4 : 0));
;         *(u32x4*)(t.WT + (size_t)row * t.K + k0 + 8 * c) = o; }
; template <int GRP> __device__ __forceinline__ void tr_group(const Params& p, unsigned char* ws, LAS float* scr, int lane, int start, int stride) {
;     ...
;     while (g < N) { const int g2 = g + 2 * stride;
;         if (g2 < N) { const TrItem tn = tr_decode(p, ws, tr_index<GRP>(g2)); tr_load(tn, nx2, lane); }
;         const TrItem tc = tr_decode(p, ws, tr_index<GRP>(g)); tr_finish(tc, cur, scr, lane);
; #pragma unroll
;         for (int i = 0; i < 32; ++i) { cur[i] = nx1[i]; nx1[i] = nx2[i]; }
;         g += stride; }
	s_waitcnt lgkmcnt(2)
	ds_read2_b32 v[14:15], v78 offset0:148 offset1:156
	ds_read2_b32 v[16:17], v78 offset0:181 offset1:189
	v_cvt_pk_bf16_f32 v2, v8, v6
	s_waitcnt lgkmcnt(3)
	s_waitcnt lgkmcnt(2)
	ds_read2_b32 v[18:19], v78 offset0:214 offset1:222
	ds_read2_b32 v[20:21], v78 offset0:247 offset1:255
	v_cvt_pk_bf16_f32 v3, v10, v12
	s_waitcnt lgkmcnt(3)
	s_waitcnt lgkmcnt(2)
	v_cvt_pk_bf16_f32 v4, v14, v16
	s_waitcnt lgkmcnt(1)
	s_waitcnt lgkmcnt(0)
	v_cvt_pk_bf16_f32 v5, v18, v20
	v_or_b32_e32 v6, v26, v80
	v_lshlrev_b32_e32 v8, 1, v6
	v_and_b32_e32 v8, 0xffffffe8, v8
	v_or3_b32 v8, v77, v8, v114
	v_cndmask_b32_e64 v6, v8, v6, s[16:17]
	v_ashrrev_i32_e32 v8, 31, v6
	v_mul_lo_u32 v8, v38, v8
	v_mul_lo_u32 v10, v39, v6
	v_mad_u64_u32 v[22:23], s[18:19], v38, v6, 0
	v_add3_u32 v23, v23, v8, v10
	v_lshl_add_u64 v[22:23], v[22:23], 1, v[36:37]
	v_lshl_add_u64 v[22:23], v[22:23], 0, v[24:25]
	v_lshl_add_u64 v[22:23], v[22:23], 0, v[0:1]
	global_store_dwordx4 v[22:23], v[2:5], off
	v_bfe_u32 v6, v21, 16, 1
	v_add3_u32 v6, v21, v6, s79
	v_cvt_pk_bf16_f32 v2, v9, v7
	v_cvt_pk_bf16_f32 v3, v11, v13
	v_cvt_pk_bf16_f32 v4, v15, v17
	v_bfe_u32 v5, v19, 16, 1
	v_add3_u32 v5, v19, v5, s79
	v_lshrrev_b32_e32 v5, 16, v5
	v_and_or_b32 v5, v6, s89, v5
	v_or_b32_e32 v6, v26, v81
	v_lshlrev_b32_e32 v7, 1, v6
	v_and_b32_e32 v7, -8, v7
	v_or3_b32 v7, v77, v7, v114
	v_cndmask_b32_e64 v6, v7, v6, s[16:17]
	v_ashrrev_i32_e32 v7, 31, v6
	v_mul_lo_u32 v8, v38, v7
	v_mul_lo_u32 v9, v39, v6
	v_mad_u64_u32 v[6:7], s[16:17], v38, v6, 0
	v_add3_u32 v7, v7, v8, v9
	v_lshl_add_u64 v[6:7], v[6:7], 1, v[36:37]
	v_lshl_add_u64 v[6:7], v[6:7], 0, v[24:25]
	v_lshl_add_u64 v[6:7], v[6:7], 0, v[0:1]
	global_store_dwordx4 v[6:7], v[2:5], off
	s_waitcnt lgkmcnt(0)
	s_movk_i32 s16, 0x17ff
	v_cmp_lt_i32_e32 vcc, s16, v42
	v_mov_b32_e32 v2, v43
	v_mov_b32_e32 v3, v44
	v_mov_b32_e32 v4, v45
	v_mov_b32_e32 v5, v46
	v_mov_b32_e32 v6, v47
	v_mov_b32_e32 v7, v48
	v_mov_b32_e32 v8, v49
	v_mov_b32_e32 v9, v50
	v_mov_b32_e32 v10, v51
	v_mov_b32_e32 v11, v52
	v_mov_b32_e32 v12, v53
	v_mov_b32_e32 v13, v54
	v_mov_b32_e32 v14, v55
	v_mov_b32_e32 v15, v56
	v_mov_b32_e32 v16, v57
	v_mov_b32_e32 v17, v58
	v_mov_b32_e32 v18, v59
	v_mov_b32_e32 v19, v60
	v_mov_b32_e32 v20, v61
	v_mov_b32_e32 v21, v62
	v_mov_b32_e32 v22, v63
	v_mov_b32_e32 v23, v64
	v_mov_b32_e32 v24, v65
	v_mov_b32_e32 v25, v66
	v_mov_b32_e32 v26, v67
	v_mov_b32_e32 v27, v68
	v_mov_b32_e32 v28, v69
	v_mov_b32_e32 v29, v70
	v_mov_b32_e32 v30, v71
	v_mov_b32_e32 v31, v72
	v_mov_b32_e32 v32, v73
	v_mov_b32_e32 v33, v74
	s_or_b64 s[10:11], vcc, s[10:11]
	v_mov_b32_e32 v74, v113
	v_mov_b32_e32 v73, v112
	v_mov_b32_e32 v72, v111
	v_mov_b32_e32 v71, v110
	v_mov_b32_e32 v70, v109
	v_mov_b32_e32 v69, v108
	v_mov_b32_e32 v68, v107
	v_mov_b32_e32 v67, v106
	v_mov_b32_e32 v66, v105
	v_mov_b32_e32 v65, v104
	v_mov_b32_e32 v64, v103
	v_mov_b32_e32 v63, v102
	v_mov_b32_e32 v62, v101
	v_mov_b32_e32 v61, v100
	v_mov_b32_e32 v60, v99
	v_mov_b32_e32 v59, v98
	v_mov_b32_e32 v58, v97
	v_mov_b32_e32 v57, v96
	v_mov_b32_e32 v56, v95
	v_mov_b32_e32 v55, v94
	v_mov_b32_e32 v54, v93
	v_mov_b32_e32 v53, v92
	v_mov_b32_e32 v52, v91
	v_mov_b32_e32 v51, v90
	v_mov_b32_e32 v50, v89
	v_mov_b32_e32 v49, v88
	v_mov_b32_e32 v48, v87
	v_mov_b32_e32 v47, v86
	v_mov_b32_e32 v46, v85
	v_mov_b32_e32 v45, v84
	v_mov_b32_e32 v44, v83
	v_mov_b32_e32 v43, v35
	s_andn2_b64 exec, exec, s[10:11]
	s_cbranch_execz .LBB0_727

; __device__ __forceinline__ unsigned pk2(float lo, float hi) { return (unsigned)f2bf(lo) | ((unsigned)f2bf(hi) << 16); }
; __device__ __forceinline__ float frsq(float x) { return __builtin_amdgcn_rsqf(x); }
; __device__ __forceinline__ void ln_affine(f32x4 (&v)[4], const LnPar& q) {
;     float s = 0.f;
; #pragma unroll
;     for (int j = 0; j < 4; ++j) s += (v[j][0] + v[j][1]) + (v[j][2] + v[j][3]);
;     const float mean = wave_sum(s) * (1.f / D); float s2 = 0.f;
; #pragma unroll
;     for (int j = 0; j < 4; ++j) { v[j] = v[j] - mean; s2 += (v[j][0] * v[j][0] + v[j][1] * v[j][1]) + (v[j][2] * v[j][2] + v[j][3] * v[j][3]); }
;     const float rstd = frsq(wave_sum(s2) * (1.f / D) + 1e-5f);
; #pragma unroll
;     for (int j = 0; j < 4; ++j) v[j] = v[j] * rstd * q.g[j] + q.b[j];
; }
; __device__ __forceinline__ void store_row_bf16(bf16_t* row, const f32x4 (&v)[4], int lane) {
; #pragma unroll
;     for (int j = 0; j < 4; ++j) { u32x2 w; w.x = pk2(v[j][0], v[j][1]); w.y = pk2(v[j][2], v[j][3]); *(u32x2*)(row + 4 * lane + 256 * j) = w; }
; }
; __device__ __forceinline__ void ph_ln1(const Params& p, int l, LAS unsigned char* lds, const int wvid) {
;     ...
;         ln_affine(v, ln1);
;         store_row_bf16(HB + (size_t)r * D, v, lane);
.LBB0_1078:
	s_or_b64 exec, exec, s[0:1]
	v_pk_add_f32 v[64:65], v[66:67], v[34:35]
	v_add_f32_e32 v75, v62, v63
	v_add_f32_e32 v0, v64, v65
	v_pk_add_f32 v[64:65], v[68:69], v[36:37]
	v_add_f32_e32 v77, 0, v0
	v_pk_add_f32 v[64:65], v[64:65], v[64:65] op_sel_hi:[0,1]
	v_add_f32_e32 v79, v60, v61
	v_mov_b32_e32 v73, v65
	v_pk_add_f32 v[70:71], v[74:75], v[78:79]
	v_pk_add_f32 v[64:65], v[72:73], v[76:77]
	ds_read_b128 v[118:121], v39
	ds_read_b128 v[122:125], v39 offset:4096
	ds_read_b128 v[126:129], v39 offset:8192
	ds_read_b128 v[130:133], v39 offset:12288
	ds_read_b128 v[134:137], v39 offset:16384
	ds_read_b128 v[138:141], v39 offset:20480
	ds_read_b128 v[142:145], v39 offset:24576
	ds_read_b128 v[146:149], v39 offset:28672
	ds_read_b128 v[232:235], v39 offset:32768
	ds_read_b128 v[236:239], v39 offset:36864
	ds_read_b128 v[240:243], v39 offset:40960
	ds_read_b128 v[244:247], v39 offset:45056
	v_pk_add_f32 v[64:65], v[70:71], v[64:65]
	s_nop 0
	v_add_f32_e32 v0, v64, v65
	v_mov_b32_e32 v64, v1
	s_nop 0
	v_add_f32_dpp v0, v0, v0 quad_perm:[1,0,3,2] row_mask:0xf bank_mask:0xf bound_ctrl:1
	s_nop 1
	v_add_f32_dpp v0, v0, v0 quad_perm:[2,3,0,1] row_mask:0xf bank_mask:0xf bound_ctrl:1
	s_nop 1
	v_add_f32_dpp v0, v0, v0 row_half_mirror row_mask:0xf bank_mask:0xf bound_ctrl:1
	s_nop 1
	v_add_f32_dpp v0, v0, v0 row_mirror row_mask:0xf bank_mask:0xf bound_ctrl:1
	s_nop 1
	v_mov_b32_dpp v64, v0 row_bcast:15 row_mask:0xa bank_mask:0xf
	v_add_f32_e32 v0, v0, v64
	v_mov_b32_e32 v64, v1
	s_nop 1
	v_mov_b32_dpp v64, v0 row_bcast:31 row_mask:0xc bank_mask:0xf
	v_add_f32_e32 v0, v0, v64
	s_nop 0
	v_readlane_b32 s0, v0, 63
	s_nop 1
	v_fmac_f32_e32 v66, s0, v220
	v_fmac_f32_e32 v35, s0, v220
	v_fmac_f32_e32 v67, s0, v220
	v_fmac_f32_e32 v34, s0, v220
	v_mov_b32_e32 v64, v67
	v_mov_b32_e32 v65, v35
	v_mov_b32_e32 v35, v66
	v_pk_mul_f32 v[70:71], v[64:65], v[64:65]
	v_pk_mul_f32 v[66:67], v[34:35], v[34:35]
	v_fmac_f32_e32 v68, s0, v220
	v_fmac_f32_e32 v37, s0, v220
	v_fmac_f32_e32 v69, s0, v220
	v_pk_mov_b32 v[80:81], v[66:67], v[70:71] op_sel:[1,0]
	v_mov_b32_e32 v67, v71
	v_fmac_f32_e32 v36, s0, v220
	v_mov_b32_e32 v70, v69
	v_mov_b32_e32 v71, v37
	v_mov_b32_e32 v37, v68
	v_pk_add_f32 v[66:67], v[80:81], v[66:67]
	v_pk_mul_f32 v[80:81], v[70:71], v[70:71]
	v_pk_mul_f32 v[68:69], v[36:37], v[36:37]
	v_fmac_f32_e32 v62, s0, v220
	v_pk_mov_b32 v[82:83], v[68:69], v[80:81] op_sel:[1,0]
	v_mov_b32_e32 v69, v81
	v_fmac_f32_e32 v63, s0, v220
	v_fmac_f32_e32 v60, s0, v220
	v_mul_f32_e32 v0, v62, v62
	v_pk_add_f32 v[68:69], v[82:83], v[68:69]
	v_fmac_f32_e32 v61, s0, v220
	v_pk_fma_f32 v[80:81], v[62:63], v[62:63], v[0:1] op_sel_hi:[1,1,0]
	v_mul_f32_e32 v0, v60, v60
	v_pk_add_f32 v[66:67], v[66:67], v[66:67] op_sel_hi:[0,1]
	v_pk_add_f32 v[68:69], v[68:69], v[68:69] op_sel_hi:[0,1]
	v_pk_fma_f32 v[82:83], v[60:61], v[60:61], v[0:1] op_sel_hi:[1,1,0]
	v_fmac_f32_e32 v76, s0, v220
	v_fmac_f32_e32 v72, s0, v220
	v_fmac_f32_e32 v78, s0, v220
	v_fmac_f32_e32 v74, s0, v220
	v_mul_f32_e32 v80, v74, v74
	v_mul_f32_e32 v82, v78, v78
	v_mul_f32_e32 v66, v72, v72
	v_mul_f32_e32 v68, v76, v76
	v_pk_add_f32 v[80:81], v[80:81], v[82:83]
	v_pk_add_f32 v[66:67], v[66:67], v[68:69]
	v_mov_b32_e32 v75, v78
	v_pk_add_f32 v[66:67], v[80:81], v[66:67]
	v_mov_b32_e32 v73, v76
	v_add_f32_e32 v0, v66, v67
	v_mov_b32_e32 v66, v1
	s_nop 0
	v_add_f32_dpp v0, v0, v0 quad_perm:[1,0,3,2] row_mask:0xf bank_mask:0xf bound_ctrl:1
	s_nop 1
	v_add_f32_dpp v0, v0, v0 quad_perm:[2,3,0,1] row_mask:0xf bank_mask:0xf bound_ctrl:1
	s_nop 1
	v_add_f32_dpp v0, v0, v0 row_half_mirror row_mask:0xf bank_mask:0xf bound_ctrl:1
	s_nop 1
	v_add_f32_dpp v0, v0, v0 row_mirror row_mask:0xf bank_mask:0xf bound_ctrl:1
	s_nop 1
	v_mov_b32_dpp v66, v0 row_bcast:15 row_mask:0xa bank_mask:0xf
	v_add_f32_e32 v0, v0, v66
	v_mov_b32_e32 v66, v1
	s_nop 1
	v_mov_b32_dpp v66, v0 row_bcast:31 row_mask:0xc bank_mask:0xf
	v_add_f32_e32 v0, v0, v66
	s_nop 0
	v_readlane_b32 s0, v0, 63
	s_nop 1
	v_fma_f32 v0, s0, v221, v204
	v_rsq_f32_e32 v0, v0
	s_nop 0
	v_pk_mul_f32 v[34:35], v[34:35], v[0:1] op_sel_hi:[1,0]
	s_nop 0
	v_pk_fma_f32 v[94:95], v[30:31], v[34:35], v[22:23]
	v_pk_mul_f32 v[34:35], v[36:37], v[0:1] op_sel_hi:[1,0]
	v_pk_mul_f32 v[36:37], v[70:71], v[0:1] op_sel_hi:[1,0]
	v_pk_mul_f32 v[64:65], v[64:65], v[0:1] op_sel_hi:[1,0]
	v_pk_fma_f32 v[68:69], v[28:29], v[36:37], v[20:21]
	v_pk_fma_f32 v[70:71], v[26:27], v[34:35], v[18:19]
	v_pk_mul_f32 v[34:35], v[62:63], v[0:1] op_sel_hi:[1,0]
	v_pk_mul_f32 v[36:37], v[60:61], v[0:1] op_sel_hi:[1,0]
	v_pk_fma_f32 v[92:93], v[32:33], v[64:65], v[24:25]
	v_pk_fma_f32 v[64:65], v[16:17], v[36:37], v[8:9]
	v_pk_fma_f32 v[66:67], v[14:15], v[34:35], v[6:7]
	v_pk_mul_f32 v[34:35], v[74:75], v[0:1] op_sel_hi:[1,0]
	v_pk_mul_f32 v[36:37], v[72:73], v[0:1] op_sel_hi:[1,0]
	v_bfe_u32 v0, v94, 16, 1
	v_pk_fma_f32 v[62:63], v[10:11], v[34:35], v[2:3]
	v_add3_u32 v0, v94, v0, s79
	v_bfe_u32 v34, v95, 16, 1
	v_lshrrev_b32_e32 v0, 16, v0
	v_add3_u32 v34, v95, v34, s79
	v_and_or_b32 v34, v34, s89, v0
	v_cvt_pk_bf16_f32 v35, v92, v93
	v_bfe_u32 v0, v70, 16, 1
	global_store_dwordx2 v[58:59], v[34:35], off offset:-1536
	v_add3_u32 v0, v70, v0, s79
	v_bfe_u32 v34, v71, 16, 1
	v_lshrrev_b32_e32 v0, 16, v0
	v_add3_u32 v34, v71, v34, s79
	v_and_or_b32 v34, v34, s89, v0
	v_cvt_pk_bf16_f32 v35, v68, v69
	v_bfe_u32 v0, v66, 16, 1
	global_store_dwordx2 v[58:59], v[34:35], off offset:-1024
	v_add3_u32 v0, v66, v0, s79
	v_bfe_u32 v34, v67, 16, 1
	v_lshrrev_b32_e32 v0, 16, v0
	v_add3_u32 v34, v67, v34, s79
	v_and_or_b32 v34, v34, s89, v0
	v_cvt_pk_bf16_f32 v35, v64, v65
	v_bfe_u32 v0, v62, 16, 1
	global_store_dwordx2 v[58:59], v[34:35], off offset:-512
	v_add3_u32 v0, v62, v0, s79
	v_bfe_u32 v34, v63, 16, 1
	v_pk_fma_f32 v[60:61], v[12:13], v[36:37], v[4:5]
	v_lshrrev_b32_e32 v0, 16, v0
	v_add3_u32 v34, v63, v34, s79
	v_and_or_b32 v34, v34, s89, v0
	v_cvt_pk_bf16_f32 v35, v60, v61
	global_store_dwordx2 v[58:59], v[34:35], off
	s_waitcnt lgkmcnt(11)
; #define LAS __attribute__((address_space(3)))
; __device__ __forceinline__ void ph_ln1(const Params& p, int l, LAS unsigned char* lds, const int wvid) {
;     ...
; #pragma unroll
;         for (int j = 0; j < 4; ++j)
; #pragma unroll
;             for (int e = 0; e < 16; ++e) { const f32x4 w = *(const LAS f32x4*)(rw + e * D + 256 * j + 4 * lane);
;                 lg[e] += (v[j][0] * w[0] + v[j][1] * w[1]) + (v[j][2] * w[2] + v[j][3] * w[3]); }
	v_mul_f32_e32 v0, v119, v95
	v_fmac_f32_e32 v0, v118, v94
	v_mul_f32_e32 v34, v121, v93
	v_fmac_f32_e32 v34, v120, v92
	ds_read_b128 v[118:121], v39 offset:49152
	v_add_f32_e32 v0, v0, v34
	v_add_f32_e32 v72, 0, v0
	s_waitcnt lgkmcnt(11)
	v_mul_f32_e32 v0, v123, v95
	v_fmac_f32_e32 v0, v122, v94
	v_mul_f32_e32 v34, v125, v93
	v_fmac_f32_e32 v34, v124, v92
	ds_read_b128 v[122:125], v39 offset:53248
	v_add_f32_e32 v0, v0, v34
	v_add_f32_e32 v73, 0, v0
	s_waitcnt lgkmcnt(11)
	v_mul_f32_e32 v0, v95, v127
	v_fmac_f32_e32 v0, v94, v126
	v_mul_f32_e32 v34, v93, v129
	v_fmac_f32_e32 v34, v92, v128
	ds_read_b128 v[126:129], v39 offset:57344
	v_add_f32_e32 v0, v0, v34
	v_add_f32_e32 v75, 0, v0
	s_waitcnt lgkmcnt(11)
	v_mul_f32_e32 v0, v95, v131
	v_fmac_f32_e32 v0, v94, v130
	v_mul_f32_e32 v34, v93, v133
	v_fmac_f32_e32 v34, v92, v132
	ds_read_b128 v[130:133], v39 offset:61440
	v_add_f32_e32 v0, v0, v34
	v_add_f32_e32 v77, 0, v0
	s_waitcnt lgkmcnt(11)
	v_mul_f32_e32 v0, v95, v135
	v_fmac_f32_e32 v0, v94, v134
	v_mul_f32_e32 v34, v93, v137
	v_fmac_f32_e32 v34, v92, v136
	ds_read_b128 v[134:137], v39 offset:1024
	v_add_f32_e32 v0, v0, v34
	v_add_f32_e32 v79, 0, v0
	s_waitcnt lgkmcnt(11)
	v_mul_f32_e32 v0, v95, v139
	v_fmac_f32_e32 v0, v94, v138
	v_mul_f32_e32 v34, v93, v141
	v_fmac_f32_e32 v34, v92, v140
	ds_read_b128 v[138:141], v39 offset:5120
	v_add_f32_e32 v0, v0, v34
	v_add_f32_e32 v81, 0, v0
	s_waitcnt lgkmcnt(11)
	v_mul_f32_e32 v0, v95, v143
	v_fmac_f32_e32 v0, v94, v142
	v_mul_f32_e32 v34, v93, v145
	v_fmac_f32_e32 v34, v92, v144
	ds_read_b128 v[142:145], v39 offset:9216
	v_add_f32_e32 v0, v0, v34
	v_add_f32_e32 v82, 0, v0
	s_waitcnt lgkmcnt(11)
	v_mul_f32_e32 v0, v95, v147
	v_fmac_f32_e32 v0, v94, v146
	v_mul_f32_e32 v34, v93, v149
	v_fmac_f32_e32 v34, v92, v148
	ds_read_b128 v[146:149], v39 offset:13312
	v_add_f32_e32 v0, v0, v34
	v_add_f32_e32 v80, 0, v0
	s_waitcnt lgkmcnt(11)
	v_mul_f32_e32 v0, v95, v233
	v_fmac_f32_e32 v0, v94, v232
	v_mul_f32_e32 v34, v93, v235
	v_fmac_f32_e32 v34, v92, v234
	ds_read_b128 v[232:235], v39 offset:17408
	v_add_f32_e32 v0, v0, v34
	v_add_f32_e32 v78, 0, v0
	s_waitcnt lgkmcnt(11)
	v_mul_f32_e32 v0, v95, v237
	v_fmac_f32_e32 v0, v94, v236
	v_mul_f32_e32 v34, v93, v239
	v_fmac_f32_e32 v34, v92, v238
	ds_read_b128 v[236:239], v39 offset:21504
	v_add_f32_e32 v0, v0, v34
	v_add_f32_e32 v76, 0, v0
	s_waitcnt lgkmcnt(11)
	v_mul_f32_e32 v0, v95, v241
	v_fmac_f32_e32 v0, v94, v240
	v_mul_f32_e32 v34, v93, v243
	v_fmac_f32_e32 v34, v92, v242
	ds_read_b128 v[240:243], v39 offset:25600
	v_add_f32_e32 v0, v0, v34
	v_add_f32_e32 v74, 0, v0
	s_waitcnt lgkmcnt(11)
	v_mul_f32_e32 v0, v95, v245
	v_fmac_f32_e32 v0, v94, v244
	v_mul_f32_e32 v34, v93, v247
	v_fmac_f32_e32 v34, v92, v246
	ds_read_b128 v[244:247], v39 offset:29696
	v_add_f32_e32 v0, v0, v34
	v_add_f32_e32 v37, 0, v0
	s_waitcnt lgkmcnt(11)
	v_mul_f32_e32 v0, v95, v119
	v_mul_f32_e32 v34, v93, v121
	v_fmac_f32_e32 v0, v94, v118
	v_fmac_f32_e32 v34, v92, v120
	ds_read_b128 v[118:121], v39 offset:33792
	v_add_f32_e32 v0, v0, v34
	v_add_f32_e32 v36, 0, v0
	s_waitcnt lgkmcnt(11)
	v_mul_f32_e32 v0, v95, v123
	v_mul_f32_e32 v34, v93, v125
	v_fmac_f32_e32 v0, v94, v122
	v_fmac_f32_e32 v34, v92, v124
	ds_read_b128 v[122:125], v39 offset:37888
	v_add_f32_e32 v0, v0, v34
	v_add_f32_e32 v35, 0, v0
	s_waitcnt lgkmcnt(11)
	v_mul_f32_e32 v0, v95, v127
	v_mul_f32_e32 v34, v93, v129
	v_fmac_f32_e32 v0, v94, v126
	v_fmac_f32_e32 v34, v92, v128
	ds_read_b128 v[126:129], v39 offset:41984
	v_add_f32_e32 v0, v0, v34
	v_add_f32_e32 v34, 0, v0
	s_waitcnt lgkmcnt(11)
	v_mul_f32_e32 v0, v95, v131
	v_mul_f32_e32 v83, v93, v133
	v_fmac_f32_e32 v0, v94, v130
	v_fmac_f32_e32 v83, v92, v132
	ds_read_b128 v[130:133], v39 offset:46080
	v_add_f32_e32 v0, v0, v83
	v_add_f32_e32 v0, 0, v0
	s_waitcnt lgkmcnt(11)
	v_mul_f32_e32 v83, v71, v135
	v_fmac_f32_e32 v83, v70, v134
	v_mul_f32_e32 v88, v69, v137
	v_fmac_f32_e32 v88, v68, v136
	ds_read_b128 v[134:137], v39 offset:50176
	v_add_f32_e32 v83, v83, v88
	v_add_f32_e32 v72, v72, v83
	s_waitcnt lgkmcnt(11)
	v_mul_f32_e32 v83, v71, v139
	v_fmac_f32_e32 v83, v70, v138
	v_mul_f32_e32 v88, v69, v141
	v_fmac_f32_e32 v88, v68, v140
	ds_read_b128 v[138:141], v39 offset:54272
	v_add_f32_e32 v83, v83, v88
	v_add_f32_e32 v73, v73, v83
	s_waitcnt lgkmcnt(11)
	v_mul_f32_e32 v83, v71, v143
	v_fmac_f32_e32 v83, v70, v142
	v_mul_f32_e32 v88, v69, v145
	v_fmac_f32_e32 v88, v68, v144
	ds_read_b128 v[142:145], v39 offset:58368
	v_add_f32_e32 v83, v83, v88
	v_add_f32_e32 v75, v75, v83
	s_waitcnt lgkmcnt(11)
	v_mul_f32_e32 v83, v71, v147
	v_fmac_f32_e32 v83, v70, v146
	v_mul_f32_e32 v88, v69, v149
	v_fmac_f32_e32 v88, v68, v148
	ds_read_b128 v[146:149], v39 offset:62464
	v_add_f32_e32 v83, v83, v88
	v_add_f32_e32 v77, v77, v83
	s_waitcnt lgkmcnt(11)
	v_mul_f32_e32 v83, v71, v233
	v_fmac_f32_e32 v83, v70, v232
	v_mul_f32_e32 v88, v69, v235
	v_fmac_f32_e32 v88, v68, v234
	ds_read_b128 v[232:235], v39 offset:2048
	v_add_f32_e32 v83, v83, v88
	v_add_f32_e32 v79, v79, v83
	s_waitcnt lgkmcnt(11)
	v_mul_f32_e32 v83, v71, v237
	v_fmac_f32_e32 v83, v70, v236
	v_mul_f32_e32 v88, v69, v239
	v_fmac_f32_e32 v88, v68, v238
	ds_read_b128 v[236:239], v39 offset:6144
	v_add_f32_e32 v83, v83, v88
	v_add_f32_e32 v81, v81, v83
	s_waitcnt lgkmcnt(11)
	v_mul_f32_e32 v83, v71, v241
	v_fmac_f32_e32 v83, v70, v240
	v_mul_f32_e32 v88, v69, v243
	v_fmac_f32_e32 v88, v68, v242
	ds_read_b128 v[240:243], v39 offset:10240
	v_add_f32_e32 v83, v83, v88
	v_add_f32_e32 v82, v82, v83
	s_waitcnt lgkmcnt(11)
; #define LAS __attribute__((address_space(3)))
; __device__ __forceinline__ void ph_ln1(const Params& p, int l, LAS unsigned char* lds, const int wvid) {
;     ...
; #pragma unroll
;         for (int j = 0; j < 4; ++j)
; #pragma unroll
;             for (int e = 0; e < 16; ++e) { const f32x4 w = *(const LAS f32x4*)(rw + e * D + 256 * j + 4 * lane);
;                 lg[e] += (v[j][0] * w[0] + v[j][1] * w[1]) + (v[j][2] * w[2] + v[j][3] * w[3]); }
	v_mul_f32_e32 v83, v71, v245
	v_fmac_f32_e32 v83, v70, v244
	v_mul_f32_e32 v88, v69, v247
	v_fmac_f32_e32 v88, v68, v246
	ds_read_b128 v[244:247], v39 offset:14336
	v_add_f32_e32 v83, v83, v88
	v_add_f32_e32 v80, v80, v83
	s_waitcnt lgkmcnt(11)
	v_mul_f32_e32 v83, v71, v119
	v_fmac_f32_e32 v83, v70, v118
	v_mul_f32_e32 v88, v69, v121
	v_fmac_f32_e32 v88, v68, v120
	ds_read_b128 v[118:121], v39 offset:18432
	v_add_f32_e32 v83, v83, v88
	v_add_f32_e32 v78, v78, v83
	s_waitcnt lgkmcnt(11)
	v_mul_f32_e32 v83, v71, v123
	v_fmac_f32_e32 v83, v70, v122
	v_mul_f32_e32 v88, v69, v125
	v_fmac_f32_e32 v88, v68, v124
	ds_read_b128 v[122:125], v39 offset:22528
	v_add_f32_e32 v83, v83, v88
	v_add_f32_e32 v76, v76, v83
	s_waitcnt lgkmcnt(11)
	v_mul_f32_e32 v83, v71, v127
	v_fmac_f32_e32 v83, v70, v126
	v_mul_f32_e32 v88, v69, v129
	v_fmac_f32_e32 v88, v68, v128
	ds_read_b128 v[126:129], v39 offset:26624
	v_add_f32_e32 v83, v83, v88
	v_add_f32_e32 v88, v74, v83
	s_waitcnt lgkmcnt(11)
	v_mul_f32_e32 v83, v69, v133
	v_fmac_f32_e32 v83, v68, v132
	v_mul_f32_e32 v74, v71, v131
	v_fmac_f32_e32 v74, v70, v130
	ds_read_b128 v[130:133], v39 offset:30720
	v_add_f32_e32 v74, v74, v83
	v_add_f32_e32 v90, v37, v74
	s_waitcnt lgkmcnt(11)
	v_mul_f32_e32 v74, v69, v137
	v_fmac_f32_e32 v74, v68, v136
	v_mul_f32_e32 v37, v71, v135
	v_fmac_f32_e32 v37, v70, v134
	ds_read_b128 v[134:137], v39 offset:34816
	v_add_f32_e32 v37, v37, v74
	v_add_f32_e32 v92, v36, v37
	s_waitcnt lgkmcnt(11)
	v_mul_f32_e32 v36, v71, v139
	v_mul_f32_e32 v37, v69, v141
	v_fmac_f32_e32 v36, v70, v138
	v_fmac_f32_e32 v37, v68, v140
	ds_read_b128 v[138:141], v39 offset:38912
	v_add_f32_e32 v36, v36, v37
	v_add_f32_e32 v93, v35, v36
	s_waitcnt lgkmcnt(11)
	v_mul_f32_e32 v35, v71, v143
	v_mul_f32_e32 v36, v69, v145
	v_fmac_f32_e32 v35, v70, v142
	v_fmac_f32_e32 v36, v68, v144
	ds_read_b128 v[142:145], v39 offset:43008
	v_add_f32_e32 v35, v35, v36
	v_add_f32_e32 v94, v34, v35
	s_waitcnt lgkmcnt(11)
	v_mul_f32_e32 v35, v71, v147
	v_fmac_f32_e32 v35, v70, v146
	v_mul_f32_e32 v34, v69, v149
	v_fmac_f32_e32 v34, v68, v148
	ds_read_b128 v[146:149], v39 offset:47104
	v_add_f32_e32 v34, v35, v34
	v_add_f32_e32 v0, v0, v34
	s_waitcnt lgkmcnt(11)
	v_mul_f32_e32 v35, v67, v233
	v_fmac_f32_e32 v35, v66, v232
	v_mul_f32_e32 v34, v65, v235
	v_fmac_f32_e32 v34, v64, v234
	ds_read_b128 v[232:235], v39 offset:51200
	v_add_f32_e32 v34, v35, v34
	v_add_f32_e32 v91, v72, v34
	s_waitcnt lgkmcnt(11)
	v_mul_f32_e32 v35, v67, v237
	v_fmac_f32_e32 v35, v66, v236
	v_mul_f32_e32 v34, v65, v239
	v_fmac_f32_e32 v34, v64, v238
	ds_read_b128 v[236:239], v39 offset:55296
	v_add_f32_e32 v34, v35, v34
	v_add_f32_e32 v89, v73, v34
	s_waitcnt lgkmcnt(11)
	v_mul_f32_e32 v35, v67, v241
	v_fmac_f32_e32 v35, v66, v240
	v_mul_f32_e32 v34, v65, v243
	v_fmac_f32_e32 v34, v64, v242
	ds_read_b128 v[240:243], v39 offset:59392
	v_add_f32_e32 v34, v35, v34
	v_add_f32_e32 v83, v75, v34
	s_waitcnt lgkmcnt(11)
	v_mul_f32_e32 v35, v67, v245
	v_fmac_f32_e32 v35, v66, v244
	v_mul_f32_e32 v34, v65, v247
	v_fmac_f32_e32 v34, v64, v246
	ds_read_b128 v[244:247], v39 offset:63488
	v_add_f32_e32 v34, v35, v34
	v_add_f32_e32 v75, v77, v34
	s_waitcnt lgkmcnt(11)
	v_mul_f32_e32 v35, v67, v119
	v_fmac_f32_e32 v35, v66, v118
	v_mul_f32_e32 v34, v65, v121
	v_fmac_f32_e32 v34, v64, v120
	ds_read_b128 v[118:121], v39 offset:3072
	v_add_f32_e32 v34, v35, v34
	v_add_f32_e32 v72, v79, v34
	s_waitcnt lgkmcnt(11)
	v_mul_f32_e32 v35, v67, v123
	v_fmac_f32_e32 v35, v66, v122
	v_mul_f32_e32 v34, v65, v125
	v_fmac_f32_e32 v34, v64, v124
	ds_read_b128 v[122:125], v39 offset:7168
	v_add_f32_e32 v34, v35, v34
	v_add_f32_e32 v74, v81, v34
	s_waitcnt lgkmcnt(11)
	v_mul_f32_e32 v35, v67, v127
	v_fmac_f32_e32 v35, v66, v126
	v_mul_f32_e32 v34, v65, v129
	v_fmac_f32_e32 v34, v64, v128
	ds_read_b128 v[126:129], v39 offset:11264
	v_add_f32_e32 v34, v35, v34
	v_add_f32_e32 v73, v82, v34
	s_waitcnt lgkmcnt(11)
	v_mul_f32_e32 v35, v67, v131
	v_fmac_f32_e32 v35, v66, v130
	v_mul_f32_e32 v34, v65, v133
	v_fmac_f32_e32 v34, v64, v132
	ds_read_b128 v[130:133], v39 offset:15360
	v_add_f32_e32 v34, v35, v34
	v_add_f32_e32 v71, v80, v34
	s_waitcnt lgkmcnt(11)
	v_mul_f32_e32 v35, v67, v135
	v_fmac_f32_e32 v35, v66, v134
	v_mul_f32_e32 v34, v65, v137
	v_fmac_f32_e32 v34, v64, v136
	ds_read_b128 v[134:137], v39 offset:19456
	v_add_f32_e32 v34, v35, v34
	v_add_f32_e32 v70, v78, v34
	s_waitcnt lgkmcnt(11)
	v_mul_f32_e32 v35, v67, v139
	v_fmac_f32_e32 v35, v66, v138
	v_mul_f32_e32 v34, v65, v141
	v_fmac_f32_e32 v34, v64, v140
	ds_read_b128 v[138:141], v39 offset:23552
	v_add_f32_e32 v34, v35, v34
	v_add_f32_e32 v69, v76, v34
	s_waitcnt lgkmcnt(11)
	v_mul_f32_e32 v35, v67, v143
	v_fmac_f32_e32 v35, v66, v142
	v_mul_f32_e32 v34, v65, v145
	v_fmac_f32_e32 v34, v64, v144
	ds_read_b128 v[142:145], v39 offset:27648
	v_add_f32_e32 v34, v35, v34
	v_add_f32_e32 v68, v88, v34
	s_waitcnt lgkmcnt(11)
	v_mul_f32_e32 v35, v67, v147
	v_fmac_f32_e32 v35, v66, v146
	v_mul_f32_e32 v34, v65, v149
	v_fmac_f32_e32 v34, v64, v148
	ds_read_b128 v[146:149], v39 offset:31744
	v_add_f32_e32 v34, v35, v34
	v_add_f32_e32 v37, v90, v34
	s_waitcnt lgkmcnt(11)
	v_mul_f32_e32 v34, v67, v233
	v_mul_f32_e32 v35, v65, v235
	v_fmac_f32_e32 v34, v66, v232
	v_fmac_f32_e32 v35, v64, v234
	ds_read_b128 v[232:235], v39 offset:35840
	v_add_f32_e32 v34, v34, v35
	v_add_f32_e32 v36, v92, v34
	s_waitcnt lgkmcnt(11)
	v_mul_f32_e32 v34, v67, v237
	v_mul_f32_e32 v35, v65, v239
	v_fmac_f32_e32 v34, v66, v236
	v_fmac_f32_e32 v35, v64, v238
	ds_read_b128 v[236:239], v39 offset:39936
	v_add_f32_e32 v34, v34, v35
	v_add_f32_e32 v35, v93, v34
	s_waitcnt lgkmcnt(11)
; #define LAS __attribute__((address_space(3)))
; template <int CTRL> __device__ __forceinline__ float dpp_get(float v) { return __int_as_float(__builtin_amdgcn_update_dpp(0, __float_as_int(v), CTRL, 0xF, 0xF, false)); }
; __device__ __forceinline__ void ph_ln1(const Params& p, int l, LAS unsigned char* lds, const int wvid) {
;     ...
; #pragma unroll
;         for (int j = 0; j < 4; ++j)
; #pragma unroll
;             for (int e = 0; e < 16; ++e) { const f32x4 w = *(const LAS f32x4*)(rw + e * D + 256 * j + 4 * lane);
;                 lg[e] += (v[j][0] * w[0] + v[j][1] * w[1]) + (v[j][2] * w[2] + v[j][3] * w[3]); }
;         { const bool b3 = lane & 8, b2 = lane & 4, b1 = lane & 2, b0 = lane & 1;
;           float h8[8], h4[4], h2[2];
; #pragma unroll
;           for (int i = 0; i < 8; ++i) h8[i] = (b3 ? lg[i + 8] : lg[i]) + dpp_get<0x128>(b3 ? lg[i] : lg[i + 8]);
; #pragma unroll
;           for (int i = 0; i < 4; ++i) h4[i] = (b2 ? h8[i + 4] : h8[i]) + dpp_get<0x141>(b2 ? h8[i] : h8[i + 4]);
; #pragma unroll
;           for (int i = 0; i < 2; ++i) h2[i] = (b1 ? h4[i + 2] : h4[i]) + dpp_get<0x4E>(b1 ? h4[i] : h4[i + 2]);
;           float x = (b0 ? h2[1] : h2[0]) + dpp_get<0xB1>(b0 ? h2[0] : h2[1]);
;           x += __shfl_xor(x, 16); x += __shfl_xor(x, 32);
;           if (lane < 16) LG[(wave * 20 + k) * 16 + lane] = x; }
	v_mul_f32_e32 v34, v67, v241
	v_fmac_f32_e32 v34, v66, v240
	v_mul_f32_e32 v76, v65, v243
	v_fmac_f32_e32 v76, v64, v242
	ds_read_b128 v[240:243], v39 offset:44032
	v_add_f32_e32 v34, v34, v76
	v_add_f32_e32 v34, v94, v34
	s_waitcnt lgkmcnt(11)
	v_mul_f32_e32 v67, v67, v245
	v_mul_f32_e32 v65, v65, v247
	v_fmac_f32_e32 v67, v66, v244
	v_fmac_f32_e32 v65, v64, v246
	ds_read_b128 v[244:247], v39 offset:48128
	v_add_f32_e32 v64, v67, v65
	v_add_f32_e32 v0, v0, v64
	s_waitcnt lgkmcnt(11)
	v_mul_f32_e32 v65, v63, v119
	v_fmac_f32_e32 v65, v62, v118
	v_mul_f32_e32 v64, v61, v121
	v_fmac_f32_e32 v64, v60, v120
	ds_read_b128 v[118:121], v39 offset:52224
	v_add_f32_e32 v64, v65, v64
	s_waitcnt lgkmcnt(11)
	v_mul_f32_e32 v65, v63, v123
	v_mul_f32_e32 v66, v61, v125
	v_fmac_f32_e32 v65, v62, v122
	v_fmac_f32_e32 v66, v60, v124
	ds_read_b128 v[122:125], v39 offset:56320
	v_add_f32_e32 v65, v65, v66
	v_add_f32_e32 v64, v91, v64
	v_add_f32_e32 v65, v89, v65
	s_waitcnt lgkmcnt(11)
	v_mul_f32_e32 v66, v63, v127
	v_mul_f32_e32 v67, v61, v129
	v_fmac_f32_e32 v66, v62, v126
	v_fmac_f32_e32 v67, v60, v128
	ds_read_b128 v[126:129], v39 offset:60416
	v_add_f32_e32 v66, v66, v67
	v_add_f32_e32 v66, v83, v66
	s_waitcnt lgkmcnt(11)
	v_mul_f32_e32 v67, v63, v131
	v_fmac_f32_e32 v67, v62, v130
	v_mul_f32_e32 v76, v61, v133
	v_fmac_f32_e32 v76, v60, v132
	ds_read_b128 v[130:133], v39 offset:64512
	v_add_f32_e32 v67, v67, v76
	v_add_f32_e32 v67, v75, v67
	s_waitcnt lgkmcnt(11)
	v_mul_f32_e32 v75, v63, v135
	v_fmac_f32_e32 v75, v62, v134
	v_mul_f32_e32 v76, v61, v137
	v_fmac_f32_e32 v76, v60, v136
	v_add_f32_e32 v75, v75, v76
	v_add_f32_e32 v72, v72, v75
	s_waitcnt lgkmcnt(10)
	v_mul_f32_e32 v75, v63, v139
	v_fmac_f32_e32 v75, v62, v138
	v_mul_f32_e32 v76, v61, v141
	v_fmac_f32_e32 v76, v60, v140
	v_add_f32_e32 v75, v75, v76
	v_add_f32_e32 v74, v74, v75
	s_waitcnt lgkmcnt(9)
	v_mul_f32_e32 v75, v63, v143
	v_fmac_f32_e32 v75, v62, v142
	v_mul_f32_e32 v76, v61, v145
	v_fmac_f32_e32 v76, v60, v144
	v_add_f32_e32 v75, v75, v76
	v_add_f32_e32 v73, v73, v75
	s_waitcnt lgkmcnt(8)
	v_mul_f32_e32 v75, v63, v147
	v_fmac_f32_e32 v75, v62, v146
	v_mul_f32_e32 v76, v61, v149
	v_fmac_f32_e32 v76, v60, v148
	v_add_f32_e32 v75, v75, v76
	v_add_f32_e32 v71, v71, v75
	s_waitcnt lgkmcnt(7)
	v_mul_f32_e32 v75, v63, v233
	v_fmac_f32_e32 v75, v62, v232
	v_mul_f32_e32 v76, v61, v235
	v_fmac_f32_e32 v76, v60, v234
	v_add_f32_e32 v75, v75, v76
	v_add_f32_e32 v70, v70, v75
	s_waitcnt lgkmcnt(6)
	v_mul_f32_e32 v75, v63, v237
	v_fmac_f32_e32 v75, v62, v236
	v_mul_f32_e32 v76, v61, v239
	v_fmac_f32_e32 v76, v60, v238
	v_add_f32_e32 v75, v75, v76
	v_add_f32_e32 v69, v69, v75
	s_waitcnt lgkmcnt(5)
	v_mul_f32_e32 v75, v63, v241
	v_fmac_f32_e32 v75, v62, v240
	v_mul_f32_e32 v76, v61, v243
	v_fmac_f32_e32 v76, v60, v242
	v_add_f32_e32 v75, v75, v76
	v_add_f32_e32 v68, v68, v75
	s_waitcnt lgkmcnt(4)
	v_mul_f32_e32 v75, v63, v245
	v_fmac_f32_e32 v75, v62, v244
	v_mul_f32_e32 v76, v61, v247
	v_fmac_f32_e32 v76, v60, v246
	v_add_f32_e32 v75, v75, v76
	v_add_f32_e32 v75, v37, v75
	s_waitcnt lgkmcnt(3)
	v_mul_f32_e32 v37, v63, v119
	v_fmac_f32_e32 v37, v62, v118
	v_mul_f32_e32 v76, v61, v121
	v_fmac_f32_e32 v76, v60, v120
	v_add_f32_e32 v37, v37, v76
	v_add_f32_e32 v80, v36, v37
	s_waitcnt lgkmcnt(2)
	v_mul_f32_e32 v36, v63, v123
	v_mul_f32_e32 v37, v61, v125
	v_fmac_f32_e32 v36, v62, v122
	v_fmac_f32_e32 v37, v60, v124
	v_add_f32_e32 v36, v36, v37
	v_add_f32_e32 v81, v35, v36
	s_waitcnt lgkmcnt(1)
	v_mul_f32_e32 v35, v63, v127
	v_mul_f32_e32 v36, v61, v129
	v_fmac_f32_e32 v35, v62, v126
	v_fmac_f32_e32 v36, v60, v128
	v_add_f32_e32 v35, v35, v36
	v_add_f32_e32 v76, v34, v35
	s_waitcnt lgkmcnt(0)
	v_mul_f32_e32 v35, v63, v131
	v_fmac_f32_e32 v35, v62, v130
	v_mul_f32_e32 v34, v61, v133
	v_fmac_f32_e32 v34, v60, v132
	v_add_f32_e32 v34, v35, v34
	v_add_f32_e32 v0, v0, v34
	v_cndmask_b32_e32 v34, v70, v64, vcc
	v_cndmask_b32_e32 v35, v64, v70, vcc
	v_cndmask_b32_e32 v36, v65, v69, vcc
	v_cndmask_b32_e32 v37, v66, v68, vcc
	v_add_f32_dpp v34, v35, v34 row_ror:8 row_mask:0xf bank_mask:0xf bound_ctrl:1
	v_cndmask_b32_e32 v35, v69, v65, vcc
	v_cndmask_b32_e32 v60, v67, v75, vcc
	v_cndmask_b32_e32 v61, v72, v80, vcc
	v_add_f32_dpp v35, v36, v35 row_ror:8 row_mask:0xf bank_mask:0xf bound_ctrl:1
	v_cndmask_b32_e32 v36, v68, v66, vcc
	v_cndmask_b32_e32 v62, v74, v81, vcc
	v_cndmask_b32_e32 v63, v73, v76, vcc
	v_add_f32_dpp v36, v37, v36 row_ror:8 row_mask:0xf bank_mask:0xf bound_ctrl:1
	v_cndmask_b32_e32 v37, v75, v67, vcc
	s_nop 1
	v_add_f32_dpp v37, v60, v37 row_ror:8 row_mask:0xf bank_mask:0xf bound_ctrl:1
	v_cndmask_b32_e32 v60, v80, v72, vcc
	s_nop 1
	v_add_f32_dpp v60, v61, v60 row_ror:8 row_mask:0xf bank_mask:0xf bound_ctrl:1
	v_cndmask_b32_e32 v61, v81, v74, vcc
	s_nop 1
	v_add_f32_dpp v61, v62, v61 row_ror:8 row_mask:0xf bank_mask:0xf bound_ctrl:1
	v_cndmask_b32_e32 v62, v76, v73, vcc
	s_nop 1
	v_add_f32_dpp v62, v63, v62 row_ror:8 row_mask:0xf bank_mask:0xf bound_ctrl:1
	v_cndmask_b32_e32 v63, v0, v71, vcc
	v_cndmask_b32_e32 v0, v71, v0, vcc
	s_nop 1
	v_add_f32_dpp v0, v0, v63 row_ror:8 row_mask:0xf bank_mask:0xf bound_ctrl:1
	v_cndmask_b32_e64 v63, v60, v34, s[4:5]
	v_cndmask_b32_e64 v34, v34, v60, s[4:5]
	v_cndmask_b32_e64 v60, v61, v35, s[4:5]
	v_cndmask_b32_e64 v35, v35, v61, s[4:5]
	v_add_f32_dpp v34, v34, v63 row_half_mirror row_mask:0xf bank_mask:0xf bound_ctrl:1
	s_nop 0
	v_add_f32_dpp v35, v35, v60 row_half_mirror row_mask:0xf bank_mask:0xf bound_ctrl:1
	v_cndmask_b32_e64 v60, v62, v36, s[4:5]
	v_cndmask_b32_e64 v36, v36, v62, s[4:5]
	s_nop 1
	v_add_f32_dpp v36, v36, v60 row_half_mirror row_mask:0xf bank_mask:0xf bound_ctrl:1
	v_cndmask_b32_e64 v60, v0, v37, s[4:5]
	v_cndmask_b32_e64 v0, v37, v0, s[4:5]
	v_cndmask_b32_e64 v37, v36, v34, s[6:7]
	v_cndmask_b32_e64 v34, v34, v36, s[6:7]
	v_add_f32_dpp v0, v0, v60 row_half_mirror row_mask:0xf bank_mask:0xf bound_ctrl:1
	v_cndmask_b32_e64 v36, v0, v35, s[6:7]
	v_cndmask_b32_e64 v0, v35, v0, s[6:7]
	v_add_f32_dpp v34, v34, v37 quad_perm:[2,3,0,1] row_mask:0xf bank_mask:0xf bound_ctrl:1
	s_nop 0
	v_add_f32_dpp v0, v0, v36 quad_perm:[2,3,0,1] row_mask:0xf bank_mask:0xf bound_ctrl:1
	v_cndmask_b32_e64 v35, v0, v34, s[8:9]
	v_cndmask_b32_e64 v0, v34, v0, s[8:9]
	s_nop 1
	v_add_f32_dpp v0, v0, v35 quad_perm:[1,0,3,2] row_mask:0xf bank_mask:0xf bound_ctrl:1
	ds_bpermute_b32 v34, v43, v0
	s_waitcnt lgkmcnt(0)
	v_add_f32_e32 v0, v0, v34
	ds_bpermute_b32 v34, v85, v0
	s_and_saveexec_b64 s[0:1], s[10:11]
	s_cbranch_execz .LBB0_1073
	s_waitcnt lgkmcnt(0)
	v_add_f32_e32 v0, v0, v34
	ds_write_b32 v86, v0
	s_branch .LBB0_1073

; #define LAS __attribute__((address_space(3)))
; __device__ __forceinline__ unsigned pk2(float lo, float hi) { return (unsigned)f2bf(lo) | ((unsigned)f2bf(hi) << 16); }
; __device__ __forceinline__ void tr_finish(const TrItem& t, const float (&v)[32], LAS float* scr, int lane) {
;     const int nblk = t.N / 32, kb = t.item / nblk, nb = t.item % nblk, k0 = 64 * kb, n0 = 32 * nb;
; #pragma unroll
;     for (int i = 0; i < 32; ++i) scr[(2 * i + (lane >> 5)) * 33 + (lane & 31)] = v[i];
;     asm volatile("s_waitcnt lgkmcnt(0)" ::: "memory");
;     const int c = lane & 7;
; #pragma unroll
;     for (int j = 0; j < 4; ++j) { const int n = (lane >> 3) + 8 * j; const LAS float* s = scr + (8 * c) * 33 + n;
;         u32x4 o; o.x = pk2(s[0 * 33], s[1 * 33]); o.y = pk2(s[2 * 33], s[3 * 33]); o.z = pk2(s[4 * 33], s[5 * 33]); o.w = pk2(s[6 * 33], s[7 * 33]);
;         const int ng = n0 + n; const int row = t.mode == 0 ? ng : (8 * (ng >> 2) + (ng & 3) + (t.mode == 2 ? 4 : 0));
;         *(u32x4*)(t.WT + (size_t)row * t.K + k0 + 8 * c) = o; }
.LBB0_1273:
	s_or_b64 exec, exec, s[22:23]
	v_cvt_f32_i32_sdwa v40, sext(v116) dst_sel:DWORD dst_unused:UNUSED_PAD src0_sel:WORD_0
	v_cvt_f32_i32_sdwa v117, sext(v115) dst_sel:DWORD dst_unused:UNUSED_PAD src0_sel:WORD_0
	s_waitcnt vmcnt(0)
	ds_write2_b32 v82, v2, v3 offset1:66
	v_xor_b32_sdwa v41, sext(v115), sext(v116) dst_sel:DWORD dst_unused:UNUSED_PAD src0_sel:WORD_0 src1_sel:WORD_0
	v_rcp_iflag_f32_e32 v2, v40
	ds_write2_b32 v82, v4, v5 offset0:132 offset1:198
	v_ashrrev_i32_e32 v3, 30, v41
	v_or_b32_e32 v3, 1, v3
	v_mul_f32_e32 v2, v117, v2
	v_trunc_f32_e32 v2, v2
	v_cvt_i32_f32_e32 v4, v2
	v_fma_f32 v2, -v2, v40, v117
	v_cmp_ge_f32_e64 vcc, |v2|, |v40|
	v_add_u32_e32 v42, s31, v42
	s_nop 0
	v_cndmask_b32_e32 v2, 0, v3, vcc
	v_add_u32_e32 v2, v4, v2
	v_mov_b32_e32 v3, 6
	v_lshlrev_b32_sdwa v40, v3, sext(v2) dst_sel:DWORD dst_unused:UNUSED_PAD src0_sel:DWORD src1_sel:WORD_0
	v_add_u32_e32 v3, 0x400, v82
	ds_write2_b32 v3, v6, v7 offset0:8 offset1:74
	ds_write2_b32 v3, v8, v9 offset0:140 offset1:206
	v_add_u32_e32 v3, 0x800, v82
	ds_write2_b32 v3, v10, v11 offset0:16 offset1:82
	ds_write2_b32 v3, v12, v13 offset0:148 offset1:214
	v_add_u32_e32 v3, 0xc00, v82
	ds_write2_b32 v3, v14, v15 offset0:24 offset1:90
	ds_write2_b32 v3, v16, v17 offset0:156 offset1:222
	v_add_u32_e32 v3, 0x1000, v82
	ds_write2_b32 v3, v18, v19 offset0:32 offset1:98
	ds_write2_b32 v3, v20, v21 offset0:164 offset1:230
	v_add_u32_e32 v3, 0x1400, v82
	ds_write2_b32 v3, v22, v23 offset0:40 offset1:106
	ds_write2_b32 v3, v24, v25 offset0:172 offset1:238
	v_add_u32_e32 v3, 0x1800, v82
	ds_write2_b32 v3, v26, v27 offset0:48 offset1:114
	ds_write2_b32 v3, v28, v29 offset0:180 offset1:246
	v_add_u32_e32 v3, 0x1c00, v82
	ds_write2_b32 v3, v30, v31 offset0:56 offset1:122
	ds_write2_b32 v3, v32, v33 offset0:188 offset1:254
	s_waitcnt lgkmcnt(0)
	ds_read2_b32 v[6:7], v78 offset1:8
	ds_read2_b32 v[8:9], v78 offset0:33 offset1:41
	v_mul_lo_u16_e32 v2, v2, v116
	ds_read2_b32 v[10:11], v78 offset0:66 offset1:74
	v_sub_u16_e32 v2, v115, v2
	ds_read2_b32 v[12:13], v78 offset0:99 offset1:107
	v_lshlrev_b32_sdwa v26, v252, sext(v2) dst_sel:DWORD dst_unused:UNUSED_PAD src0_sel:DWORD src1_sel:WORD_0
	s_waitcnt lgkmcnt(3)
	s_waitcnt lgkmcnt(2)
	ds_read2_b32 v[14:15], v78 offset0:132 offset1:140
	ds_read2_b32 v[16:17], v78 offset0:165 offset1:173
	v_cvt_pk_bf16_f32 v2, v6, v8
	s_waitcnt lgkmcnt(3)
	s_waitcnt lgkmcnt(2)
	ds_read2_b32 v[18:19], v78 offset0:198 offset1:206
	ds_read2_b32 v[20:21], v78 offset0:231 offset1:239
	v_cvt_pk_bf16_f32 v3, v10, v12
	s_waitcnt lgkmcnt(3)
	s_waitcnt lgkmcnt(2)
	v_cvt_pk_bf16_f32 v4, v14, v16
	s_waitcnt lgkmcnt(1)
	s_waitcnt lgkmcnt(0)
	v_cvt_pk_bf16_f32 v5, v18, v20
	v_or_b32_e32 v6, v26, v76
	v_lshlrev_b32_e32 v8, 1, v6
	v_and_b32_e32 v8, 0xffffffc8, v8
	v_or3_b32 v8, v77, v8, v114
	v_cndmask_b32_e64 v6, v8, v6, s[20:21]
	v_ashrrev_i32_e32 v8, 31, v6
	v_mul_lo_u32 v8, v38, v8
	v_mul_lo_u32 v10, v39, v6
	v_mad_u64_u32 v[22:23], s[22:23], v38, v6, 0
	v_ashrrev_i32_e32 v41, 31, v40
	v_add3_u32 v23, v23, v8, v10
	v_lshl_add_u64 v[22:23], v[22:23], 1, v[36:37]
	v_lshlrev_b64 v[24:25], 1, v[40:41]
	v_lshl_add_u64 v[22:23], v[22:23], 0, v[24:25]
	v_lshl_add_u64 v[22:23], v[22:23], 0, v[0:1]
	global_store_dwordx4 v[22:23], v[2:5], off
	v_bfe_u32 v6, v21, 16, 1
	v_add3_u32 v6, v21, v6, s79
	v_cvt_pk_bf16_f32 v2, v7, v9
	v_cvt_pk_bf16_f32 v3, v11, v13
	v_cvt_pk_bf16_f32 v4, v15, v17
	v_bfe_u32 v5, v19, 16, 1
	v_add3_u32 v5, v19, v5, s79
	v_lshrrev_b32_e32 v5, 16, v5
	v_and_or_b32 v5, v6, s89, v5
	v_or_b32_e32 v6, v26, v79
	v_lshlrev_b32_e32 v7, 1, v6
	v_and_b32_e32 v7, 0xffffffd8, v7
	v_or3_b32 v7, v77, v7, v114
	v_cndmask_b32_e64 v6, v7, v6, s[20:21]
	v_ashrrev_i32_e32 v7, 31, v6
	v_mul_lo_u32 v8, v38, v7
	v_mul_lo_u32 v9, v39, v6
	v_mad_u64_u32 v[6:7], s[22:23], v38, v6, 0
	v_add3_u32 v7, v7, v8, v9
	v_lshl_add_u64 v[6:7], v[6:7], 1, v[36:37]
	v_lshl_add_u64 v[6:7], v[6:7], 0, v[24:25]
	ds_read2_b32 v[8:9], v78 offset0:16 offset1:24
	v_lshl_add_u64 v[6:7], v[6:7], 0, v[0:1]
	global_store_dwordx4 v[6:7], v[2:5], off
	ds_read2_b32 v[6:7], v78 offset0:49 offset1:57
	ds_read2_b32 v[10:11], v78 offset0:82 offset1:90
	ds_read2_b32 v[12:13], v78 offset0:115 offset1:123
	s_waitcnt lgkmcnt(3)
; #define LAS __attribute__((address_space(3)))
; __device__ __forceinline__ unsigned pk2(float lo, float hi) { return (unsigned)f2bf(lo) | ((unsigned)f2bf(hi) << 16); }
; __device__ __forceinline__ void tr_finish(const TrItem& t, const float (&v)[32], LAS float* scr, int lane) {
;     ...
;     for (int j = 0; j < 4; ++j) { const int n = (lane >> 3) + 8 * j; const LAS float* s = scr + (8 * c) * 33 + n;
;         u32x4 o; o.x = pk2(s[0 * 33], s[1 * 33]); o.y = pk2(s[2 * 33], s[3 * 33]); o.z = pk2(s[4 * 33], s[5 * 33]); o.w = pk2(s[6 * 33], s[7 * 33]);
;         const int ng = n0 + n; const int row = t.mode == 0 ? ng : (8 * (ng >> 2) + (ng & 3) + (t.mode == 2 ? 4 : 0));
;         *(u32x4*)(t.WT + (size_t)row * t.K + k0 + 8 * c) = o; }
; template <int GRP> __device__ __forceinline__ void tr_group(const Params& p, unsigned char* ws, LAS float* scr, int lane, int start, int stride) {
;     ...
;     while (g < N) { const int g2 = g + 2 * stride;
;         if (g2 < N) { const TrItem tn = tr_decode(p, ws, tr_index<GRP>(g2)); tr_load(tn, nx2, lane); }
;         const TrItem tc = tr_decode(p, ws, tr_index<GRP>(g)); tr_finish(tc, cur, scr, lane);
; #pragma unroll
;         for (int i = 0; i < 32; ++i) { cur[i] = nx1[i]; nx1[i] = nx2[i]; }
;         g += stride; }
	s_waitcnt lgkmcnt(2)
	ds_read2_b32 v[14:15], v78 offset0:148 offset1:156
	ds_read2_b32 v[16:17], v78 offset0:181 offset1:189
	v_cvt_pk_bf16_f32 v2, v8, v6
	s_waitcnt lgkmcnt(3)
	s_waitcnt lgkmcnt(2)
	ds_read2_b32 v[18:19], v78 offset0:214 offset1:222
	ds_read2_b32 v[20:21], v78 offset0:247 offset1:255
	v_cvt_pk_bf16_f32 v3, v10, v12
	s_waitcnt lgkmcnt(3)
	s_waitcnt lgkmcnt(2)
	v_cvt_pk_bf16_f32 v4, v14, v16
	s_waitcnt lgkmcnt(1)
	s_waitcnt lgkmcnt(0)
	v_cvt_pk_bf16_f32 v5, v18, v20
	v_or_b32_e32 v6, v26, v80
	v_lshlrev_b32_e32 v8, 1, v6
	v_and_b32_e32 v8, 0xffffffe8, v8
	v_or3_b32 v8, v77, v8, v114
	v_cndmask_b32_e64 v6, v8, v6, s[20:21]
	v_ashrrev_i32_e32 v8, 31, v6
	v_mul_lo_u32 v8, v38, v8
	v_mul_lo_u32 v10, v39, v6
	v_mad_u64_u32 v[22:23], s[22:23], v38, v6, 0
	v_add3_u32 v23, v23, v8, v10
	v_lshl_add_u64 v[22:23], v[22:23], 1, v[36:37]
	v_lshl_add_u64 v[22:23], v[22:23], 0, v[24:25]
	v_lshl_add_u64 v[22:23], v[22:23], 0, v[0:1]
	global_store_dwordx4 v[22:23], v[2:5], off
	v_bfe_u32 v6, v21, 16, 1
	v_add3_u32 v6, v21, v6, s79
	v_cvt_pk_bf16_f32 v2, v9, v7
	v_cvt_pk_bf16_f32 v3, v11, v13
	v_cvt_pk_bf16_f32 v4, v15, v17
	v_bfe_u32 v5, v19, 16, 1
	v_add3_u32 v5, v19, v5, s79
	v_lshrrev_b32_e32 v5, 16, v5
	v_and_or_b32 v5, v6, s89, v5
	v_or_b32_e32 v6, v26, v81
	v_lshlrev_b32_e32 v7, 1, v6
	v_and_b32_e32 v7, -8, v7
	v_or3_b32 v7, v77, v7, v114
	v_cndmask_b32_e64 v6, v7, v6, s[20:21]
	v_ashrrev_i32_e32 v7, 31, v6
	v_mul_lo_u32 v8, v38, v7
	v_mul_lo_u32 v9, v39, v6
	v_mad_u64_u32 v[6:7], s[20:21], v38, v6, 0
	v_add3_u32 v7, v7, v8, v9
	v_lshl_add_u64 v[6:7], v[6:7], 1, v[36:37]
	v_lshl_add_u64 v[6:7], v[6:7], 0, v[24:25]
	v_lshl_add_u64 v[6:7], v[6:7], 0, v[0:1]
	global_store_dwordx4 v[6:7], v[2:5], off
	s_waitcnt lgkmcnt(0)
	s_movk_i32 s20, 0xfff
	v_cmp_lt_i32_e32 vcc, s20, v42
	v_mov_b32_e32 v2, v43
	v_mov_b32_e32 v3, v44
	v_mov_b32_e32 v4, v45
	v_mov_b32_e32 v5, v46
	v_mov_b32_e32 v6, v47
	v_mov_b32_e32 v7, v48
	v_mov_b32_e32 v8, v49
	v_mov_b32_e32 v9, v50
	v_mov_b32_e32 v10, v51
	v_mov_b32_e32 v11, v52
	v_mov_b32_e32 v12, v53
	v_mov_b32_e32 v13, v54
	v_mov_b32_e32 v14, v55
	v_mov_b32_e32 v15, v56
	v_mov_b32_e32 v16, v57
	v_mov_b32_e32 v17, v58
	v_mov_b32_e32 v18, v59
	v_mov_b32_e32 v19, v60
	v_mov_b32_e32 v20, v61
	v_mov_b32_e32 v21, v62
	v_mov_b32_e32 v22, v63
	v_mov_b32_e32 v23, v64
	v_mov_b32_e32 v24, v65
	v_mov_b32_e32 v25, v66
	v_mov_b32_e32 v26, v67
	v_mov_b32_e32 v27, v68
	v_mov_b32_e32 v28, v69
	v_mov_b32_e32 v29, v70
	v_mov_b32_e32 v30, v71
	v_mov_b32_e32 v31, v72
	v_mov_b32_e32 v32, v73
	v_mov_b32_e32 v33, v74
	s_or_b64 s[18:19], vcc, s[18:19]
	v_mov_b32_e32 v74, v113
	v_mov_b32_e32 v73, v112
	v_mov_b32_e32 v72, v111
	v_mov_b32_e32 v71, v110
	v_mov_b32_e32 v70, v109
	v_mov_b32_e32 v69, v108
	v_mov_b32_e32 v68, v107
	v_mov_b32_e32 v67, v106
	v_mov_b32_e32 v66, v105
	v_mov_b32_e32 v65, v104
	v_mov_b32_e32 v64, v103
	v_mov_b32_e32 v63, v102
	v_mov_b32_e32 v62, v101
	v_mov_b32_e32 v61, v100
	v_mov_b32_e32 v60, v99
	v_mov_b32_e32 v59, v98
	v_mov_b32_e32 v58, v97
	v_mov_b32_e32 v57, v96
	v_mov_b32_e32 v56, v95
	v_mov_b32_e32 v55, v94
	v_mov_b32_e32 v54, v93
	v_mov_b32_e32 v53, v92
	v_mov_b32_e32 v52, v91
	v_mov_b32_e32 v51, v90
	v_mov_b32_e32 v50, v89
	v_mov_b32_e32 v49, v88
	v_mov_b32_e32 v48, v87
	v_mov_b32_e32 v47, v86
	v_mov_b32_e32 v46, v85
	v_mov_b32_e32 v45, v84
	v_mov_b32_e32 v44, v83
	v_mov_b32_e32 v43, v35
	s_andn2_b64 exec, exec, s[18:19]
	s_cbranch_execz .LBB0_1308

; #define LAS __attribute__((address_space(3)))
; __device__ __forceinline__ unsigned pk2(float lo, float hi) { return (unsigned)f2bf(lo) | ((unsigned)f2bf(hi) << 16); }
; __device__ __forceinline__ void tr_finish(const TrItem& t, const float (&v)[32], LAS float* scr, int lane) {
;     const int nblk = t.N / 32, kb = t.item / nblk, nb = t.item % nblk, k0 = 64 * kb, n0 = 32 * nb;
; #pragma unroll
;     for (int i = 0; i < 32; ++i) scr[(2 * i + (lane >> 5)) * 33 + (lane & 31)] = v[i];
;     asm volatile("s_waitcnt lgkmcnt(0)" ::: "memory");
;     const int c = lane & 7;
; #pragma unroll
;     for (int j = 0; j < 4; ++j) { const int n = (lane >> 3) + 8 * j; const LAS float* s = scr + (8 * c) * 33 + n;
;         u32x4 o; o.x = pk2(s[0 * 33], s[1 * 33]); o.y = pk2(s[2 * 33], s[3 * 33]); o.z = pk2(s[4 * 33], s[5 * 33]); o.w = pk2(s[6 * 33], s[7 * 33]);
;         const int ng = n0 + n; const int row = t.mode == 0 ? ng : (8 * (ng >> 2) + (ng & 3) + (t.mode == 2 ? 4 : 0));
;         *(u32x4*)(t.WT + (size_t)row * t.K + k0 + 8 * c) = o; }
.LBB0_1358:
	s_or_b64 exec, exec, s[18:19]
	v_cvt_f32_i32_sdwa v40, sext(v116) dst_sel:DWORD dst_unused:UNUSED_PAD src0_sel:WORD_0
	v_cvt_f32_i32_sdwa v117, sext(v115) dst_sel:DWORD dst_unused:UNUSED_PAD src0_sel:WORD_0
	s_waitcnt vmcnt(30)
	ds_write2_b32 v82, v2, v3 offset1:66
	v_xor_b32_sdwa v41, sext(v115), sext(v116) dst_sel:DWORD dst_unused:UNUSED_PAD src0_sel:WORD_0 src1_sel:WORD_0
	v_rcp_iflag_f32_e32 v2, v40
	s_waitcnt vmcnt(28)
	ds_write2_b32 v82, v4, v5 offset0:132 offset1:198
	v_ashrrev_i32_e32 v3, 30, v41
	v_or_b32_e32 v3, 1, v3
	v_mul_f32_e32 v2, v117, v2
	v_trunc_f32_e32 v2, v2
	v_cvt_i32_f32_e32 v4, v2
	v_fma_f32 v2, -v2, v40, v117
	v_cmp_ge_f32_e64 vcc, |v2|, |v40|
	v_add_u32_e32 v42, s26, v42
	s_nop 0
	v_cndmask_b32_e32 v2, 0, v3, vcc
	v_add_u32_e32 v2, v4, v2
	v_mov_b32_e32 v3, 6
	v_lshlrev_b32_sdwa v40, v3, sext(v2) dst_sel:DWORD dst_unused:UNUSED_PAD src0_sel:DWORD src1_sel:WORD_0
	v_add_u32_e32 v3, 0x400, v82
	s_waitcnt vmcnt(26)
	ds_write2_b32 v3, v6, v7 offset0:8 offset1:74
	s_waitcnt vmcnt(24)
	ds_write2_b32 v3, v8, v9 offset0:140 offset1:206
	v_add_u32_e32 v3, 0x800, v82
	s_waitcnt vmcnt(22)
	ds_write2_b32 v3, v10, v11 offset0:16 offset1:82
	s_waitcnt vmcnt(20)
	ds_write2_b32 v3, v12, v13 offset0:148 offset1:214
	v_add_u32_e32 v3, 0xc00, v82
	s_waitcnt vmcnt(18)
	ds_write2_b32 v3, v14, v15 offset0:24 offset1:90
	s_waitcnt vmcnt(16)
	ds_write2_b32 v3, v16, v17 offset0:156 offset1:222
	v_add_u32_e32 v3, 0x1000, v82
	s_waitcnt vmcnt(14)
	ds_write2_b32 v3, v18, v19 offset0:32 offset1:98
	s_waitcnt vmcnt(12)
	ds_write2_b32 v3, v20, v21 offset0:164 offset1:230
	v_add_u32_e32 v3, 0x1400, v82
	s_waitcnt vmcnt(10)
	ds_write2_b32 v3, v22, v23 offset0:40 offset1:106
	s_waitcnt vmcnt(8)
	ds_write2_b32 v3, v24, v25 offset0:172 offset1:238
	v_add_u32_e32 v3, 0x1800, v82
	s_waitcnt vmcnt(6)
	ds_write2_b32 v3, v26, v27 offset0:48 offset1:114
	s_waitcnt vmcnt(4)
	ds_write2_b32 v3, v28, v29 offset0:180 offset1:246
	v_add_u32_e32 v3, 0x1c00, v82
	s_waitcnt vmcnt(2)
	ds_write2_b32 v3, v30, v31 offset0:56 offset1:122
	s_waitcnt vmcnt(0)
	ds_write2_b32 v3, v32, v33 offset0:188 offset1:254
	s_waitcnt lgkmcnt(0)
	ds_read2_b32 v[6:7], v78 offset1:8
	ds_read2_b32 v[8:9], v78 offset0:33 offset1:41
	v_mul_lo_u16_e32 v2, v2, v116
	ds_read2_b32 v[10:11], v78 offset0:66 offset1:74
	v_sub_u16_e32 v2, v115, v2
	ds_read2_b32 v[12:13], v78 offset0:99 offset1:107
	v_lshlrev_b32_sdwa v26, v252, sext(v2) dst_sel:DWORD dst_unused:UNUSED_PAD src0_sel:DWORD src1_sel:WORD_0
	s_waitcnt lgkmcnt(3)
	s_waitcnt lgkmcnt(2)
	ds_read2_b32 v[14:15], v78 offset0:132 offset1:140
	ds_read2_b32 v[16:17], v78 offset0:165 offset1:173
	v_cvt_pk_bf16_f32 v2, v6, v8
	s_waitcnt lgkmcnt(3)
	s_waitcnt lgkmcnt(2)
	ds_read2_b32 v[18:19], v78 offset0:198 offset1:206
	ds_read2_b32 v[20:21], v78 offset0:231 offset1:239
	v_cvt_pk_bf16_f32 v3, v10, v12
	s_waitcnt lgkmcnt(3)
	s_waitcnt lgkmcnt(2)
	v_cvt_pk_bf16_f32 v4, v14, v16
	s_waitcnt lgkmcnt(1)
	s_waitcnt lgkmcnt(0)
	v_cvt_pk_bf16_f32 v5, v18, v20
	v_or_b32_e32 v6, v26, v76
	v_lshlrev_b32_e32 v8, 1, v6
	v_and_b32_e32 v8, 0xffffffc8, v8
	v_or3_b32 v8, v77, v8, v114
	v_cndmask_b32_e64 v6, v8, v6, s[16:17]
	v_ashrrev_i32_e32 v8, 31, v6
	v_mul_lo_u32 v8, v38, v8
	v_mul_lo_u32 v10, v39, v6
	v_mad_u64_u32 v[22:23], s[18:19], v38, v6, 0
	v_ashrrev_i32_e32 v41, 31, v40
	v_add3_u32 v23, v23, v8, v10
	v_lshl_add_u64 v[22:23], v[22:23], 1, v[36:37]
	v_lshlrev_b64 v[24:25], 1, v[40:41]
	v_lshl_add_u64 v[22:23], v[22:23], 0, v[24:25]
	v_lshl_add_u64 v[22:23], v[22:23], 0, v[0:1]
	global_store_dwordx4 v[22:23], v[2:5], off
	v_bfe_u32 v6, v21, 16, 1
	v_add3_u32 v6, v21, v6, s79
	v_cvt_pk_bf16_f32 v2, v7, v9
	v_cvt_pk_bf16_f32 v3, v11, v13
	v_cvt_pk_bf16_f32 v4, v15, v17
	v_bfe_u32 v5, v19, 16, 1
	v_add3_u32 v5, v19, v5, s79
	v_lshrrev_b32_e32 v5, 16, v5
	v_and_or_b32 v5, v6, s89, v5
	v_or_b32_e32 v6, v26, v79
	v_lshlrev_b32_e32 v7, 1, v6
	v_and_b32_e32 v7, 0xffffffd8, v7
	v_or3_b32 v7, v77, v7, v114
	v_cndmask_b32_e64 v6, v7, v6, s[16:17]
	v_ashrrev_i32_e32 v7, 31, v6
	v_mul_lo_u32 v8, v38, v7
	v_mul_lo_u32 v9, v39, v6
	v_mad_u64_u32 v[6:7], s[18:19], v38, v6, 0
	v_add3_u32 v7, v7, v8, v9
	v_lshl_add_u64 v[6:7], v[6:7], 1, v[36:37]
	v_lshl_add_u64 v[6:7], v[6:7], 0, v[24:25]
	ds_read2_b32 v[8:9], v78 offset0:16 offset1:24
	v_lshl_add_u64 v[6:7], v[6:7], 0, v[0:1]
	global_store_dwordx4 v[6:7], v[2:5], off
	ds_read2_b32 v[6:7], v78 offset0:49 offset1:57
	ds_read2_b32 v[10:11], v78 offset0:82 offset1:90
	ds_read2_b32 v[12:13], v78 offset0:115 offset1:123
	s_waitcnt lgkmcnt(3)
; #define LAS __attribute__((address_space(3)))
; __device__ __forceinline__ unsigned pk2(float lo, float hi) { return (unsigned)f2bf(lo) | ((unsigned)f2bf(hi) << 16); }
; __device__ __forceinline__ void tr_finish(const TrItem& t, const float (&v)[32], LAS float* scr, int lane) {
;     ...
;     for (int j = 0; j < 4; ++j) { const int n = (lane >> 3) + 8 * j; const LAS float* s = scr + (8 * c) * 33 + n;
;         u32x4 o; o.x = pk2(s[0 * 33], s[1 * 33]); o.y = pk2(s[2 * 33], s[3 * 33]); o.z = pk2(s[4 * 33], s[5 * 33]); o.w = pk2(s[6 * 33], s[7 * 33]);
;         const int ng = n0 + n; const int row = t.mode == 0 ? ng : (8 * (ng >> 2) + (ng & 3) + (t.mode == 2 ? 4 : 0));
;         *(u32x4*)(t.WT + (size_t)row * t.K + k0 + 8 * c) = o; }
; template <int GRP> __device__ __forceinline__ void tr_group(const Params& p, unsigned char* ws, LAS float* scr, int lane, int start, int stride) {
;     ...
;     while (g < N) { const int g2 = g + 2 * stride;
;         if (g2 < N) { const TrItem tn = tr_decode(p, ws, tr_index<GRP>(g2)); tr_load(tn, nx2, lane); }
;         const TrItem tc = tr_decode(p, ws, tr_index<GRP>(g)); tr_finish(tc, cur, scr, lane);
; #pragma unroll
;         for (int i = 0; i < 32; ++i) { cur[i] = nx1[i]; nx1[i] = nx2[i]; }
;         g += stride; }
	s_waitcnt lgkmcnt(2)
	ds_read2_b32 v[14:15], v78 offset0:148 offset1:156
	ds_read2_b32 v[16:17], v78 offset0:181 offset1:189
	v_cvt_pk_bf16_f32 v2, v8, v6
	s_waitcnt lgkmcnt(3)
	s_waitcnt lgkmcnt(2)
	ds_read2_b32 v[18:19], v78 offset0:214 offset1:222
	ds_read2_b32 v[20:21], v78 offset0:247 offset1:255
	v_cvt_pk_bf16_f32 v3, v10, v12
	s_waitcnt lgkmcnt(3)
	s_waitcnt lgkmcnt(2)
	v_cvt_pk_bf16_f32 v4, v14, v16
	s_waitcnt lgkmcnt(1)
	s_waitcnt lgkmcnt(0)
	v_cvt_pk_bf16_f32 v5, v18, v20
	v_or_b32_e32 v6, v26, v80
	v_lshlrev_b32_e32 v8, 1, v6
	v_and_b32_e32 v8, 0xffffffe8, v8
	v_or3_b32 v8, v77, v8, v114
	v_cndmask_b32_e64 v6, v8, v6, s[16:17]
	v_ashrrev_i32_e32 v8, 31, v6
	v_mul_lo_u32 v8, v38, v8
	v_mul_lo_u32 v10, v39, v6
	v_mad_u64_u32 v[22:23], s[18:19], v38, v6, 0
	v_add3_u32 v23, v23, v8, v10
	v_lshl_add_u64 v[22:23], v[22:23], 1, v[36:37]
	v_lshl_add_u64 v[22:23], v[22:23], 0, v[24:25]
	v_lshl_add_u64 v[22:23], v[22:23], 0, v[0:1]
	global_store_dwordx4 v[22:23], v[2:5], off
	v_bfe_u32 v6, v21, 16, 1
	v_add3_u32 v6, v21, v6, s79
	v_cvt_pk_bf16_f32 v2, v9, v7
	v_cvt_pk_bf16_f32 v3, v11, v13
	v_cvt_pk_bf16_f32 v4, v15, v17
	v_bfe_u32 v5, v19, 16, 1
	v_add3_u32 v5, v19, v5, s79
	v_lshrrev_b32_e32 v5, 16, v5
	v_and_or_b32 v5, v6, s89, v5
	v_or_b32_e32 v6, v26, v81
	v_lshlrev_b32_e32 v7, 1, v6
	v_and_b32_e32 v7, -8, v7
	v_or3_b32 v7, v77, v7, v114
	v_cndmask_b32_e64 v6, v7, v6, s[16:17]
	v_ashrrev_i32_e32 v7, 31, v6
	v_mul_lo_u32 v8, v38, v7
	v_mul_lo_u32 v9, v39, v6
	v_mad_u64_u32 v[6:7], s[16:17], v38, v6, 0
	v_add3_u32 v7, v7, v8, v9
	v_lshl_add_u64 v[6:7], v[6:7], 1, v[36:37]
	v_lshl_add_u64 v[6:7], v[6:7], 0, v[24:25]
	v_lshl_add_u64 v[6:7], v[6:7], 0, v[0:1]
	global_store_dwordx4 v[6:7], v[2:5], off
	s_waitcnt lgkmcnt(0)
	s_movk_i32 s16, 0x177f
	v_cmp_lt_i32_e32 vcc, s16, v42
	v_mov_b32_e32 v2, v43
	v_mov_b32_e32 v3, v44
	v_mov_b32_e32 v4, v45
	v_mov_b32_e32 v5, v46
	v_mov_b32_e32 v6, v47
	v_mov_b32_e32 v7, v48
	v_mov_b32_e32 v8, v49
	v_mov_b32_e32 v9, v50
	v_mov_b32_e32 v10, v51
	v_mov_b32_e32 v11, v52
	v_mov_b32_e32 v12, v53
	v_mov_b32_e32 v13, v54
	v_mov_b32_e32 v14, v55
	v_mov_b32_e32 v15, v56
	v_mov_b32_e32 v16, v57
	v_mov_b32_e32 v17, v58
	v_mov_b32_e32 v18, v59
	v_mov_b32_e32 v19, v60
	v_mov_b32_e32 v20, v61
	v_mov_b32_e32 v21, v62
	v_mov_b32_e32 v22, v63
	v_mov_b32_e32 v23, v64
	v_mov_b32_e32 v24, v65
	v_mov_b32_e32 v25, v66
	v_mov_b32_e32 v26, v67
	v_mov_b32_e32 v27, v68
	v_mov_b32_e32 v28, v69
	v_mov_b32_e32 v29, v70
	v_mov_b32_e32 v30, v71
	v_mov_b32_e32 v31, v72
	v_mov_b32_e32 v32, v73
	v_mov_b32_e32 v33, v74
	s_or_b64 s[10:11], vcc, s[10:11]
	v_mov_b32_e32 v74, v113
	v_mov_b32_e32 v73, v112
	v_mov_b32_e32 v72, v111
	v_mov_b32_e32 v71, v110
	v_mov_b32_e32 v70, v109
	v_mov_b32_e32 v69, v108
	v_mov_b32_e32 v68, v107
	v_mov_b32_e32 v67, v106
	v_mov_b32_e32 v66, v105
	v_mov_b32_e32 v65, v104
	v_mov_b32_e32 v64, v103
	v_mov_b32_e32 v63, v102
	v_mov_b32_e32 v62, v101
	v_mov_b32_e32 v61, v100
	v_mov_b32_e32 v60, v99
	v_mov_b32_e32 v59, v98
	v_mov_b32_e32 v58, v97
	v_mov_b32_e32 v57, v96
	v_mov_b32_e32 v56, v95
	v_mov_b32_e32 v55, v94
	v_mov_b32_e32 v54, v93
	v_mov_b32_e32 v53, v92
	v_mov_b32_e32 v52, v91
	v_mov_b32_e32 v51, v90
	v_mov_b32_e32 v50, v89
	v_mov_b32_e32 v49, v88
	v_mov_b32_e32 v48, v87
	v_mov_b32_e32 v47, v86
	v_mov_b32_e32 v46, v85
	v_mov_b32_e32 v45, v84
	v_mov_b32_e32 v44, v83
	v_mov_b32_e32 v43, v35
	s_andn2_b64 exec, exec, s[10:11]
	s_cbranch_execz .LBB0_1401

; #define LAS __attribute__((address_space(3)))
; __device__ __forceinline__ unsigned pk2(float lo, float hi) { return (unsigned)f2bf(lo) | ((unsigned)f2bf(hi) << 16); }
; __device__ __forceinline__ void tr_finish(const TrItem& t, const float (&v)[32], LAS float* scr, int lane) {
;     const int nblk = t.N / 32, kb = t.item / nblk, nb = t.item % nblk, k0 = 64 * kb, n0 = 32 * nb;
; #pragma unroll
;     for (int i = 0; i < 32; ++i) scr[(2 * i + (lane >> 5)) * 33 + (lane & 31)] = v[i];
;     asm volatile("s_waitcnt lgkmcnt(0)" ::: "memory");
;     const int c = lane & 7;
; #pragma unroll
;     for (int j = 0; j < 4; ++j) { const int n = (lane >> 3) + 8 * j; const LAS float* s = scr + (8 * c) * 33 + n;
;         u32x4 o; o.x = pk2(s[0 * 33], s[1 * 33]); o.y = pk2(s[2 * 33], s[3 * 33]); o.z = pk2(s[4 * 33], s[5 * 33]); o.w = pk2(s[6 * 33], s[7 * 33]);
;         const int ng = n0 + n; const int row = t.mode == 0 ? ng : (8 * (ng >> 2) + (ng & 3) + (t.mode == 2 ? 4 : 0));
;         *(u32x4*)(t.WT + (size_t)row * t.K + k0 + 8 * c) = o; }
.LBB0_1540:
	s_or_b64 exec, exec, s[20:21]
	v_cvt_f32_i32_sdwa v40, sext(v116) dst_sel:DWORD dst_unused:UNUSED_PAD src0_sel:WORD_0
	v_cvt_f32_i32_sdwa v117, sext(v115) dst_sel:DWORD dst_unused:UNUSED_PAD src0_sel:WORD_0
	s_waitcnt vmcnt(0)
	ds_write2_b32 v82, v2, v3 offset1:66
	v_xor_b32_sdwa v41, sext(v115), sext(v116) dst_sel:DWORD dst_unused:UNUSED_PAD src0_sel:WORD_0 src1_sel:WORD_0
	v_rcp_iflag_f32_e32 v2, v40
	ds_write2_b32 v82, v4, v5 offset0:132 offset1:198
	v_ashrrev_i32_e32 v3, 30, v41
	v_or_b32_e32 v3, 1, v3
	v_mul_f32_e32 v2, v117, v2
	v_trunc_f32_e32 v2, v2
	v_cvt_i32_f32_e32 v4, v2
	v_fma_f32 v2, -v2, v40, v117
	v_cmp_ge_f32_e64 vcc, |v2|, |v40|
	v_add_u32_e32 v42, s28, v42
	s_nop 0
	v_cndmask_b32_e32 v2, 0, v3, vcc
	v_add_u32_e32 v2, v4, v2
	v_mov_b32_e32 v3, 6
	v_lshlrev_b32_sdwa v40, v3, sext(v2) dst_sel:DWORD dst_unused:UNUSED_PAD src0_sel:DWORD src1_sel:WORD_0
	v_add_u32_e32 v3, 0x400, v82
	ds_write2_b32 v3, v6, v7 offset0:8 offset1:74
	ds_write2_b32 v3, v8, v9 offset0:140 offset1:206
	v_add_u32_e32 v3, 0x800, v82
	ds_write2_b32 v3, v10, v11 offset0:16 offset1:82
	ds_write2_b32 v3, v12, v13 offset0:148 offset1:214
	v_add_u32_e32 v3, 0xc00, v82
	ds_write2_b32 v3, v14, v15 offset0:24 offset1:90
	ds_write2_b32 v3, v16, v17 offset0:156 offset1:222
	v_add_u32_e32 v3, 0x1000, v82
	ds_write2_b32 v3, v18, v19 offset0:32 offset1:98
	ds_write2_b32 v3, v20, v21 offset0:164 offset1:230
	v_add_u32_e32 v3, 0x1400, v82
	ds_write2_b32 v3, v22, v23 offset0:40 offset1:106
	ds_write2_b32 v3, v24, v25 offset0:172 offset1:238
	v_add_u32_e32 v3, 0x1800, v82
	ds_write2_b32 v3, v26, v27 offset0:48 offset1:114
	ds_write2_b32 v3, v28, v29 offset0:180 offset1:246
	v_add_u32_e32 v3, 0x1c00, v82
	ds_write2_b32 v3, v30, v31 offset0:56 offset1:122
	ds_write2_b32 v3, v32, v33 offset0:188 offset1:254
	s_waitcnt lgkmcnt(0)
	ds_read2_b32 v[6:7], v78 offset1:8
	ds_read2_b32 v[8:9], v78 offset0:33 offset1:41
	v_mul_lo_u16_e32 v2, v2, v116
	ds_read2_b32 v[10:11], v78 offset0:66 offset1:74
	v_sub_u16_e32 v2, v115, v2
	ds_read2_b32 v[12:13], v78 offset0:99 offset1:107
	v_lshlrev_b32_sdwa v26, v252, sext(v2) dst_sel:DWORD dst_unused:UNUSED_PAD src0_sel:DWORD src1_sel:WORD_0
	s_waitcnt lgkmcnt(3)
	s_waitcnt lgkmcnt(2)
	ds_read2_b32 v[14:15], v78 offset0:132 offset1:140
	ds_read2_b32 v[16:17], v78 offset0:165 offset1:173
	v_cvt_pk_bf16_f32 v2, v6, v8
	s_waitcnt lgkmcnt(3)
	s_waitcnt lgkmcnt(2)
	ds_read2_b32 v[18:19], v78 offset0:198 offset1:206
	ds_read2_b32 v[20:21], v78 offset0:231 offset1:239
	v_cvt_pk_bf16_f32 v3, v10, v12
	s_waitcnt lgkmcnt(3)
	s_waitcnt lgkmcnt(2)
	v_cvt_pk_bf16_f32 v4, v14, v16
	s_waitcnt lgkmcnt(1)
	s_waitcnt lgkmcnt(0)
	v_cvt_pk_bf16_f32 v5, v18, v20
	v_or_b32_e32 v6, v26, v76
	v_lshlrev_b32_e32 v8, 1, v6
	v_and_b32_e32 v8, 0xffffffc8, v8
	v_or3_b32 v8, v77, v8, v114
	v_cndmask_b32_e64 v6, v8, v6, s[18:19]
	v_ashrrev_i32_e32 v8, 31, v6
	v_mul_lo_u32 v8, v38, v8
	v_mul_lo_u32 v10, v39, v6
	v_mad_u64_u32 v[22:23], s[20:21], v38, v6, 0
	v_ashrrev_i32_e32 v41, 31, v40
	v_add3_u32 v23, v23, v8, v10
	v_lshl_add_u64 v[22:23], v[22:23], 1, v[36:37]
	v_lshlrev_b64 v[24:25], 1, v[40:41]
	v_lshl_add_u64 v[22:23], v[22:23], 0, v[24:25]
	v_lshl_add_u64 v[22:23], v[22:23], 0, v[0:1]
	global_store_dwordx4 v[22:23], v[2:5], off
	v_bfe_u32 v6, v21, 16, 1
	v_add3_u32 v6, v21, v6, s79
	v_cvt_pk_bf16_f32 v2, v7, v9
	v_cvt_pk_bf16_f32 v3, v11, v13
	v_cvt_pk_bf16_f32 v4, v15, v17
	v_bfe_u32 v5, v19, 16, 1
	v_add3_u32 v5, v19, v5, s79
	v_lshrrev_b32_e32 v5, 16, v5
	v_and_or_b32 v5, v6, s89, v5
	v_or_b32_e32 v6, v26, v79
	v_lshlrev_b32_e32 v7, 1, v6
	v_and_b32_e32 v7, 0xffffffd8, v7
	v_or3_b32 v7, v77, v7, v114
	v_cndmask_b32_e64 v6, v7, v6, s[18:19]
	v_ashrrev_i32_e32 v7, 31, v6
	v_mul_lo_u32 v8, v38, v7
	v_mul_lo_u32 v9, v39, v6
	v_mad_u64_u32 v[6:7], s[20:21], v38, v6, 0
	v_add3_u32 v7, v7, v8, v9
	v_lshl_add_u64 v[6:7], v[6:7], 1, v[36:37]
	v_lshl_add_u64 v[6:7], v[6:7], 0, v[24:25]
	ds_read2_b32 v[8:9], v78 offset0:16 offset1:24
	v_lshl_add_u64 v[6:7], v[6:7], 0, v[0:1]
	global_store_dwordx4 v[6:7], v[2:5], off
	ds_read2_b32 v[6:7], v78 offset0:49 offset1:57
	ds_read2_b32 v[10:11], v78 offset0:82 offset1:90
	ds_read2_b32 v[12:13], v78 offset0:115 offset1:123
	s_waitcnt lgkmcnt(3)
; #define LAS __attribute__((address_space(3)))
; __device__ __forceinline__ unsigned pk2(float lo, float hi) { return (unsigned)f2bf(lo) | ((unsigned)f2bf(hi) << 16); }
; __device__ __forceinline__ void tr_finish(const TrItem& t, const float (&v)[32], LAS float* scr, int lane) {
;     ...
;     for (int j = 0; j < 4; ++j) { const int n = (lane >> 3) + 8 * j; const LAS float* s = scr + (8 * c) * 33 + n;
;         u32x4 o; o.x = pk2(s[0 * 33], s[1 * 33]); o.y = pk2(s[2 * 33], s[3 * 33]); o.z = pk2(s[4 * 33], s[5 * 33]); o.w = pk2(s[6 * 33], s[7 * 33]);
;         const int ng = n0 + n; const int row = t.mode == 0 ? ng : (8 * (ng >> 2) + (ng & 3) + (t.mode == 2 ? 4 : 0));
;         *(u32x4*)(t.WT + (size_t)row * t.K + k0 + 8 * c) = o; }
; template <int GRP> __device__ __forceinline__ void tr_group(const Params& p, unsigned char* ws, LAS float* scr, int lane, int start, int stride) {
;     ...
;     while (g < N) { const int g2 = g + 2 * stride;
;         if (g2 < N) { const TrItem tn = tr_decode(p, ws, tr_index<GRP>(g2)); tr_load(tn, nx2, lane); }
;         const TrItem tc = tr_decode(p, ws, tr_index<GRP>(g)); tr_finish(tc, cur, scr, lane);
; #pragma unroll
;         for (int i = 0; i < 32; ++i) { cur[i] = nx1[i]; nx1[i] = nx2[i]; }
;         g += stride; }
	s_waitcnt lgkmcnt(2)
	ds_read2_b32 v[14:15], v78 offset0:148 offset1:156
	ds_read2_b32 v[16:17], v78 offset0:181 offset1:189
	v_cvt_pk_bf16_f32 v2, v8, v6
	s_waitcnt lgkmcnt(3)
	s_waitcnt lgkmcnt(2)
	ds_read2_b32 v[18:19], v78 offset0:214 offset1:222
	ds_read2_b32 v[20:21], v78 offset0:247 offset1:255
	v_cvt_pk_bf16_f32 v3, v10, v12
	s_waitcnt lgkmcnt(3)
	s_waitcnt lgkmcnt(2)
	v_cvt_pk_bf16_f32 v4, v14, v16
	s_waitcnt lgkmcnt(1)
	s_waitcnt lgkmcnt(0)
	v_cvt_pk_bf16_f32 v5, v18, v20
	v_or_b32_e32 v6, v26, v80
	v_lshlrev_b32_e32 v8, 1, v6
	v_and_b32_e32 v8, 0xffffffe8, v8
	v_or3_b32 v8, v77, v8, v114
	v_cndmask_b32_e64 v6, v8, v6, s[18:19]
	v_ashrrev_i32_e32 v8, 31, v6
	v_mul_lo_u32 v8, v38, v8
	v_mul_lo_u32 v10, v39, v6
	v_mad_u64_u32 v[22:23], s[20:21], v38, v6, 0
	v_add3_u32 v23, v23, v8, v10
	v_lshl_add_u64 v[22:23], v[22:23], 1, v[36:37]
	v_lshl_add_u64 v[22:23], v[22:23], 0, v[24:25]
	v_lshl_add_u64 v[22:23], v[22:23], 0, v[0:1]
	global_store_dwordx4 v[22:23], v[2:5], off
	v_bfe_u32 v6, v21, 16, 1
	v_add3_u32 v6, v21, v6, s79
	v_cvt_pk_bf16_f32 v2, v9, v7
	v_cvt_pk_bf16_f32 v3, v11, v13
	v_cvt_pk_bf16_f32 v4, v15, v17
	v_bfe_u32 v5, v19, 16, 1
	v_add3_u32 v5, v19, v5, s79
	v_lshrrev_b32_e32 v5, 16, v5
	v_and_or_b32 v5, v6, s89, v5
	v_or_b32_e32 v6, v26, v81
	v_lshlrev_b32_e32 v7, 1, v6
	v_and_b32_e32 v7, -8, v7
	v_or3_b32 v7, v77, v7, v114
	v_cndmask_b32_e64 v6, v7, v6, s[18:19]
	v_ashrrev_i32_e32 v7, 31, v6
	v_mul_lo_u32 v8, v38, v7
	v_mul_lo_u32 v9, v39, v6
	v_mad_u64_u32 v[6:7], s[18:19], v38, v6, 0
	v_add3_u32 v7, v7, v8, v9
	v_lshl_add_u64 v[6:7], v[6:7], 1, v[36:37]
	v_lshl_add_u64 v[6:7], v[6:7], 0, v[24:25]
	v_lshl_add_u64 v[6:7], v[6:7], 0, v[0:1]
	global_store_dwordx4 v[6:7], v[2:5], off
	s_waitcnt lgkmcnt(0)
	v_cmp_lt_i32_e32 vcc, s34, v42
	v_mov_b32_e32 v6, v47
	v_mov_b32_e32 v2, v43
	v_mov_b32_e32 v3, v44
	v_mov_b32_e32 v4, v45
	v_mov_b32_e32 v5, v46
	v_mov_b32_e32 v7, v48
	v_mov_b32_e32 v8, v49
	v_mov_b32_e32 v9, v50
	v_mov_b32_e32 v10, v51
	v_mov_b32_e32 v11, v52
	v_mov_b32_e32 v12, v53
	v_mov_b32_e32 v13, v54
	v_mov_b32_e32 v14, v55
	v_mov_b32_e32 v15, v56
	v_mov_b32_e32 v16, v57
	v_mov_b32_e32 v17, v58
	v_mov_b32_e32 v18, v59
	v_mov_b32_e32 v19, v60
	v_mov_b32_e32 v20, v61
	v_mov_b32_e32 v21, v62
	v_mov_b32_e32 v22, v63
	v_mov_b32_e32 v23, v64
	v_mov_b32_e32 v24, v65
	v_mov_b32_e32 v25, v66
	v_mov_b32_e32 v26, v67
	v_mov_b32_e32 v27, v68
	v_mov_b32_e32 v28, v69
	v_mov_b32_e32 v29, v70
	v_mov_b32_e32 v30, v71
	v_mov_b32_e32 v31, v72
	v_mov_b32_e32 v32, v73
	v_mov_b32_e32 v33, v74
	s_or_b64 s[16:17], vcc, s[16:17]
	v_mov_b32_e32 v74, v113
	v_mov_b32_e32 v73, v112
	v_mov_b32_e32 v72, v111
	v_mov_b32_e32 v71, v110
	v_mov_b32_e32 v70, v109
	v_mov_b32_e32 v69, v108
	v_mov_b32_e32 v68, v107
	v_mov_b32_e32 v67, v106
	v_mov_b32_e32 v66, v105
	v_mov_b32_e32 v65, v104
	v_mov_b32_e32 v64, v103
	v_mov_b32_e32 v63, v102
	v_mov_b32_e32 v62, v101
	v_mov_b32_e32 v61, v100
	v_mov_b32_e32 v60, v99
	v_mov_b32_e32 v59, v98
	v_mov_b32_e32 v58, v97
	v_mov_b32_e32 v57, v96
	v_mov_b32_e32 v56, v95
	v_mov_b32_e32 v55, v94
	v_mov_b32_e32 v54, v93
	v_mov_b32_e32 v53, v92
	v_mov_b32_e32 v52, v91
	v_mov_b32_e32 v51, v90
	v_mov_b32_e32 v50, v89
	v_mov_b32_e32 v49, v88
	v_mov_b32_e32 v48, v87
	v_mov_b32_e32 v47, v86
	v_mov_b32_e32 v46, v85
	v_mov_b32_e32 v45, v84
	v_mov_b32_e32 v44, v83
	v_mov_b32_e32 v43, v35
	s_andn2_b64 exec, exec, s[16:17]
	s_cbranch_execz .LBB0_1575

; __device__ __forceinline__ unsigned pk2(float lo, float hi) { return (unsigned)f2bf(lo) | ((unsigned)f2bf(hi) << 16); }
; __device__ __forceinline__ void store_row_bf16(bf16_t* row, const f32x4 (&v)[4], int lane) {
; #pragma unroll
;     for (int j = 0; j < 4; ++j) { u32x2 w; w.x = pk2(v[j][0], v[j][1]); w.y = pk2(v[j][2], v[j][3]); *(u32x2*)(row + 4 * lane + 256 * j) = w; }
; }
; __device__ __forceinline__ void ph_ln2(const Params& p, int l, LAS unsigned char* lds, const int wvid) {
;     ...
;             ln_affine(v, ln2);
;             if (l == NLAYER - 1) { float* o = p.out + ((size_t)b * SEQ + (t - NMETA)) * D;
; #pragma unroll
;                 for (int j = 0; j < 4; ++j) *(f32x4*)(o + 4 * lane + 256 * j) = v[j]; }
;             else store_row_bf16(HB + (size_t)rr * D, v, lane); }
.LBB0_1646:
	s_andn2_b64 vcc, exec, s[18:19]
	s_cbranch_vccnz .LBB0_1648
	v_bfe_u32 v0, v46, 16, 1
	v_add3_u32 v0, v46, v0, s79
	v_bfe_u32 v46, v47, 16, 1
	v_lshrrev_b32_e32 v0, 16, v0
	v_add3_u32 v46, v47, v46, s79
	v_and_or_b32 v46, v46, s89, v0
	v_cvt_pk_bf16_f32 v47, v48, v49
	v_bfe_u32 v0, v42, 16, 1
	v_add3_u32 v0, v42, v0, s79
	v_bfe_u32 v42, v43, 16, 1
	v_lshrrev_b32_e32 v0, 16, v0
	v_add3_u32 v42, v43, v42, s79
	v_and_or_b32 v42, v42, s89, v0
	v_cvt_pk_bf16_f32 v43, v44, v45
	v_bfe_u32 v0, v34, 16, 1
	v_add3_u32 v0, v34, v0, s79
	v_bfe_u32 v34, v35, 16, 1
	v_lshrrev_b32_e32 v0, 16, v0
	v_add3_u32 v34, v35, v34, s79
	v_and_or_b32 v34, v34, s89, v0
	v_cvt_pk_bf16_f32 v35, v36, v37
	v_bfe_u32 v0, v38, 16, 1
	global_store_dwordx2 v[118:119], v[34:35], off offset:1024
	v_add3_u32 v0, v38, v0, s79
	v_bfe_u32 v34, v39, 16, 1
	v_lshrrev_b32_e32 v0, 16, v0
	v_add3_u32 v34, v39, v34, s79
	v_and_or_b32 v34, v34, s89, v0
	v_bfe_u32 v0, v40, 16, 1
	v_add3_u32 v0, v40, v0, s79
	v_bfe_u32 v35, v41, 16, 1
	v_lshrrev_b32_e32 v0, 16, v0
	v_add3_u32 v35, v41, v35, s79
	v_and_or_b32 v35, v35, s89, v0
	global_store_dwordx2 v[118:119], v[46:47], off
	global_store_dwordx2 v[118:119], v[42:43], off offset:512
	global_store_dwordx2 v[118:119], v[34:35], off offset:1536

; __device__ __forceinline__ unsigned pk2(float lo, float hi) { return (unsigned)f2bf(lo) | ((unsigned)f2bf(hi) << 16); }
; __device__ __forceinline__ void store_row_bf16(bf16_t* row, const f32x4 (&v)[4], int lane) {
; #pragma unroll
;     for (int j = 0; j < 4; ++j) { u32x2 w; w.x = pk2(v[j][0], v[j][1]); w.y = pk2(v[j][2], v[j][3]); *(u32x2*)(row + 4 * lane + 256 * j) = w; }
; }
; __device__ __forceinline__ void ph_ln2(const Params& p, int l, LAS unsigned char* lds, const int wvid) {
;     ...
;             ln_affine(v, ln2);
;             if (l == NLAYER - 1) { float* o = p.out + ((size_t)b * SEQ + (t - NMETA)) * D;
; #pragma unroll
;                 for (int j = 0; j < 4; ++j) *(f32x4*)(o + 4 * lane + 256 * j) = v[j]; }
;             else store_row_bf16(HB + (size_t)rr * D, v, lane); }
.LBB0_1651:
	s_andn2_b64 vcc, exec, s[10:11]
	s_cbranch_vccnz .LBB0_1653
	v_bfe_u32 v0, v46, 16, 1
	v_add3_u32 v0, v46, v0, s79
	v_bfe_u32 v46, v47, 16, 1
	v_lshrrev_b32_e32 v0, 16, v0
	v_add3_u32 v46, v47, v46, s79
	v_and_or_b32 v46, v46, s89, v0
	v_cvt_pk_bf16_f32 v47, v48, v49
	v_bfe_u32 v0, v42, 16, 1
	v_add3_u32 v0, v42, v0, s79
	v_bfe_u32 v42, v43, 16, 1
	v_lshrrev_b32_e32 v0, 16, v0
	v_add3_u32 v42, v43, v42, s79
	v_and_or_b32 v42, v42, s89, v0
	v_cvt_pk_bf16_f32 v43, v44, v45
	v_bfe_u32 v0, v34, 16, 1
	v_add3_u32 v0, v34, v0, s79
	v_bfe_u32 v34, v35, 16, 1
	v_lshrrev_b32_e32 v0, 16, v0
	v_add3_u32 v34, v35, v34, s79
	v_and_or_b32 v34, v34, s89, v0
	v_ashrrev_i32_e32 v99, 31, v98
	v_lshlrev_b64 v[98:99], 11, v[98:99]
	v_lshl_add_u64 v[98:99], v[52:53], 0, v[98:99]
	v_cvt_pk_bf16_f32 v35, v36, v37
	v_bfe_u32 v0, v38, 16, 1
	global_store_dwordx2 v[98:99], v[34:35], off offset:1024
	v_add3_u32 v0, v38, v0, s79
	v_bfe_u32 v34, v39, 16, 1
	v_lshrrev_b32_e32 v0, 16, v0
	v_add3_u32 v34, v39, v34, s79
	v_and_or_b32 v34, v34, s89, v0
	v_bfe_u32 v0, v40, 16, 1
	v_add3_u32 v0, v40, v0, s79
	v_bfe_u32 v35, v41, 16, 1
	v_lshrrev_b32_e32 v0, 16, v0
	v_add3_u32 v35, v41, v35, s79
	v_and_or_b32 v35, v35, s89, v0
	global_store_dwordx2 v[98:99], v[46:47], off
	global_store_dwordx2 v[98:99], v[42:43], off offset:512
	global_store_dwordx2 v[98:99], v[34:35], off offset:1536

; __device__ __forceinline__ unsigned pk2(float lo, float hi) { return (unsigned)f2bf(lo) | ((unsigned)f2bf(hi) << 16); }
; __device__ __forceinline__ void store_row_bf16(bf16_t* row, const f32x4 (&v)[4], int lane) {
; #pragma unroll
;     for (int j = 0; j < 4; ++j) { u32x2 w; w.x = pk2(v[j][0], v[j][1]); w.y = pk2(v[j][2], v[j][3]); *(u32x2*)(row + 4 * lane + 256 * j) = w; }
; }
; __device__ __forceinline__ void ph_ln2(const Params& p, int l, LAS unsigned char* lds, const int wvid) {
;     ...
;             ln_affine(v, ln2);
;             if (l == NLAYER - 1) { float* o = p.out + ((size_t)b * SEQ + (t - NMETA)) * D;
; #pragma unroll
;                 for (int j = 0; j < 4; ++j) *(f32x4*)(o + 4 * lane + 256 * j) = v[j]; }
;             else store_row_bf16(HB + (size_t)rr * D, v, lane); }
.LBB0_1656:
	s_andn2_b64 vcc, exec, s[8:9]
	s_cbranch_vccnz .LBB0_1658
	v_bfe_u32 v0, v46, 16, 1
	v_add3_u32 v0, v46, v0, s79
	v_bfe_u32 v46, v47, 16, 1
	v_lshrrev_b32_e32 v0, 16, v0
	v_add3_u32 v46, v47, v46, s79
	v_and_or_b32 v46, v46, s89, v0
	v_cvt_pk_bf16_f32 v47, v48, v49
	v_bfe_u32 v0, v42, 16, 1
	v_add3_u32 v0, v42, v0, s79
	v_bfe_u32 v42, v43, 16, 1
	v_lshrrev_b32_e32 v0, 16, v0
	v_add3_u32 v42, v43, v42, s79
	v_and_or_b32 v42, v42, s89, v0
	v_cvt_pk_bf16_f32 v43, v44, v45
	v_bfe_u32 v0, v34, 16, 1
	v_add3_u32 v0, v34, v0, s79
	v_bfe_u32 v34, v35, 16, 1
	v_lshrrev_b32_e32 v0, 16, v0
	v_add3_u32 v34, v35, v34, s79
	v_and_or_b32 v34, v34, s89, v0
	v_ashrrev_i32_e32 v73, 31, v72
	v_lshlrev_b64 v[72:73], 11, v[72:73]
	v_lshl_add_u64 v[72:73], v[52:53], 0, v[72:73]
	v_cvt_pk_bf16_f32 v35, v36, v37
	v_bfe_u32 v0, v38, 16, 1
	global_store_dwordx2 v[72:73], v[34:35], off offset:1024
	v_add3_u32 v0, v38, v0, s79
	v_bfe_u32 v34, v39, 16, 1
	v_lshrrev_b32_e32 v0, 16, v0
	v_add3_u32 v34, v39, v34, s79
	v_and_or_b32 v34, v34, s89, v0
	v_bfe_u32 v0, v40, 16, 1
	v_add3_u32 v0, v40, v0, s79
	v_bfe_u32 v35, v41, 16, 1
	v_lshrrev_b32_e32 v0, 16, v0
	v_add3_u32 v35, v41, v35, s79
	v_and_or_b32 v35, v35, s89, v0
	global_store_dwordx2 v[72:73], v[46:47], off
	global_store_dwordx2 v[72:73], v[42:43], off offset:512
	global_store_dwordx2 v[72:73], v[34:35], off offset:1536

; __device__ __forceinline__ unsigned pk2(float lo, float hi) { return (unsigned)f2bf(lo) | ((unsigned)f2bf(hi) << 16); }
; __device__ __forceinline__ void store_row_bf16(bf16_t* row, const f32x4 (&v)[4], int lane) {
; #pragma unroll
;     for (int j = 0; j < 4; ++j) { u32x2 w; w.x = pk2(v[j][0], v[j][1]); w.y = pk2(v[j][2], v[j][3]); *(u32x2*)(row + 4 * lane + 256 * j) = w; }
; }
; __device__ __forceinline__ void ph_ln2(const Params& p, int l, LAS unsigned char* lds, const int wvid) {
;     ...
;             ln_affine(v, ln2);
;             if (l == NLAYER - 1) { float* o = p.out + ((size_t)b * SEQ + (t - NMETA)) * D;
; #pragma unroll
;                 for (int j = 0; j < 4; ++j) *(f32x4*)(o + 4 * lane + 256 * j) = v[j]; }
;             else store_row_bf16(HB + (size_t)rr * D, v, lane); }
.LBB0_1661:
	s_andn2_b64 vcc, exec, s[6:7]
	s_cbranch_vccnz .LBB0_1636
	v_bfe_u32 v0, v46, 16, 1
	v_add3_u32 v0, v46, v0, s79
	v_bfe_u32 v46, v47, 16, 1
	v_lshrrev_b32_e32 v0, 16, v0
	v_add3_u32 v46, v47, v46, s79
	v_and_or_b32 v46, v46, s89, v0
	v_cvt_pk_bf16_f32 v47, v48, v49
	v_bfe_u32 v0, v42, 16, 1
	v_add3_u32 v0, v42, v0, s79
	v_bfe_u32 v42, v43, 16, 1
	v_lshrrev_b32_e32 v0, 16, v0
	v_add3_u32 v42, v43, v42, s79
	v_and_or_b32 v42, v42, s89, v0
	v_cvt_pk_bf16_f32 v43, v44, v45
	v_bfe_u32 v0, v34, 16, 1
	v_add3_u32 v0, v34, v0, s79
	v_bfe_u32 v34, v35, 16, 1
	v_lshrrev_b32_e32 v0, 16, v0
	v_add3_u32 v34, v35, v34, s79
	v_and_or_b32 v34, v34, s89, v0
	v_ashrrev_i32_e32 v59, 31, v58
	v_lshlrev_b64 v[58:59], 11, v[58:59]
	v_lshl_add_u64 v[58:59], v[52:53], 0, v[58:59]
	v_cvt_pk_bf16_f32 v35, v36, v37
	v_bfe_u32 v0, v38, 16, 1
	global_store_dwordx2 v[58:59], v[34:35], off offset:1024
	v_add3_u32 v0, v38, v0, s79
	v_bfe_u32 v34, v39, 16, 1
	v_lshrrev_b32_e32 v0, 16, v0
	v_add3_u32 v34, v39, v34, s79
	v_and_or_b32 v34, v34, s89, v0
	v_bfe_u32 v0, v40, 16, 1
	v_add3_u32 v0, v40, v0, s79
	v_bfe_u32 v35, v41, 16, 1
	v_lshrrev_b32_e32 v0, 16, v0
	v_add3_u32 v35, v41, v35, s79
	v_and_or_b32 v35, v35, s89, v0
	global_store_dwordx2 v[58:59], v[46:47], off
	global_store_dwordx2 v[58:59], v[42:43], off offset:512
	global_store_dwordx2 v[58:59], v[34:35], off offset:1536
	s_branch .LBB0_1636
